# attention v7: 5-slot V ring + waves 4-7 lag half a tile behind waves 0-3 (stagger)
# baseline (speedup 1.0000x reference)
.LBB0_733:
	s_or_b64 exec, exec, s[8:9]
	s_movk_i32 s4, 0xf0
	s_cmp_lg_u32 0, -1
	v_lshlrev_b32_e32 v39, 8, v141
	v_bitop3_b32 v80, v142, s4, v136 bitop3:0x48
	s_cselect_b32 s10, 0, 0
	v_cvt_pk_bf16_f32 v96, v134, v135
	v_cvt_pk_bf16_f32 v97, v132, v133
	v_cvt_pk_bf16_f32 v98, v130, v131
	v_cvt_pk_bf16_f32 v99, v128, v129
	v_cvt_pk_bf16_f32 v100, v126, v127
	v_cvt_pk_bf16_f32 v101, v124, v125
	v_cvt_pk_bf16_f32 v102, v122, v123
	v_cvt_pk_bf16_f32 v103, v120, v121
	v_cvt_pk_bf16_f32 v104, v70, v71
	v_cvt_pk_bf16_f32 v105, v74, v75
	v_cvt_pk_bf16_f32 v106, v64, v65
	v_cvt_pk_bf16_f32 v107, v68, v69
	v_cvt_pk_bf16_f32 v108, v60, v61
	v_cvt_pk_bf16_f32 v109, v66, v67
	v_cvt_pk_bf16_f32 v110, v56, v57
	v_cvt_pk_bf16_f32 v111, v58, v59
	v_cvt_pk_bf16_f32 v112, v112, v113
	v_cvt_pk_bf16_f32 v113, v118, v119
	v_cvt_pk_bf16_f32 v114, v114, v115
	v_cvt_pk_bf16_f32 v115, v116, v117
	v_cvt_pk_bf16_f32 v116, v78, v79
	v_cvt_pk_bf16_f32 v117, v76, v77
	v_cvt_pk_bf16_f32 v118, v72, v73
	v_cvt_pk_bf16_f32 v119, v62, v63
	v_cvt_pk_bf16_f32 v120, v52, v53
	v_cvt_pk_bf16_f32 v121, v54, v55
	v_cvt_pk_bf16_f32 v122, v46, v47
	v_cvt_pk_bf16_f32 v123, v50, v51
	v_cvt_pk_bf16_f32 v124, v44, v45
	v_cvt_pk_bf16_f32 v125, v48, v49
	v_cvt_pk_bf16_f32 v126, v40, v41
	v_cvt_pk_bf16_f32 v127, v42, v43
	v_readlane_b32 s100, v250, 8
	v_mbcnt_lo_u32_b32 v68, -1, 0
	v_mbcnt_hi_u32_b32 v68, -1, v68
	s_nop 1
	v_add_u32_e32 v69, s100, v68
	v_lshrrev_b32_e32 v70, 3, v69
	v_and_b32_e32 v71, 7, v69
	v_lshrrev_b32_e32 v72, 2, v71
	v_bfe_u32 v73, v71, 1, 1
	v_and_b32_e32 v74, 1, v71
	v_lshlrev_b32_e32 v74, 1, v74
	v_lshl_add_u32 v75, v72, 2, v74
	v_bfe_u32 v76, v70, 1, 3
	v_xor_b32_e32 v77, v75, v76
	v_add_u32_e32 v78, 1, v75
	v_xor_b32_e32 v78, v78, v76
	v_lshlrev_b32_e32 v79, 7, v70
	v_lshl_add_u32 v79, v73, 3, v79
	v_lshl_add_u32 v64, v77, 4, v79
	v_lshl_add_u32 v65, v78, 4, v79
	v_add_u32_e32 v66, 0x2000, v64
	v_add_u32_e32 v67, 0x2000, v65
	v_or_b32_e32 v81, v39, v80
	s_add_i32 s15, s10, 0x10000
	v_and_b32_e32 v82, 6, v137
	v_lshrrev_b32_e32 v84, 4, v136
	s_waitcnt vmcnt(0)
	s_waitcnt vmcnt(0)
	s_add_i32 s11, s10, 0x12000
	v_lshl_add_u32 v83, v139, 7, s10
	v_bitop3_b32 v85, v84, v82, 7 bitop3:0x6c
	v_and_b32_e32 v86, 8, v138
	v_or_b32_e32 v82, 1, v82
	v_add_u32_e32 v225, s15, v81
	s_waitcnt vmcnt(4)
	ds_write_b128 v225, v[24:27] offset:0
	v_lshlrev_b32_e32 v85, 4, v85
	v_add_u32_e32 v87, v83, v86
	v_bitop3_b32 v82, v84, v82, 7 bitop3:0x6c
	v_add3_u32 v226, v80, s11, v39
	ds_write_b128 v226, v[28:31] offset:0
	v_lshlrev_b32_e32 v82, 4, v82
	v_add_u32_e32 v227, v87, v85
	ds_write_b64 v64, v[12:13] offset:0
	v_lshrrev_b32_e32 v32, 5, v136
	v_add_u32_e32 v83, 0x2000, v83
	v_or_b32_e32 v84, v85, v86
	v_add_u32_e32 v228, v87, v82
	ds_write_b64 v65, v[14:15] offset:0
	v_xor_b32_e32 v32, v32, v137
	v_or_b32_e32 v86, v82, v86
	v_add_u32_e32 v229, v84, v83
	ds_write_b64 v66, v[4:5] offset:0
	v_lshlrev_b32_e32 v32, 4, v32
	v_add_u32_e32 v184, v86, v83
	ds_write_b64 v67, v[6:7] offset:0
	v_lshlrev_b32_e32 v33, 8, v143
	v_and_b32_e32 v32, 16, v32
	v_bfe_u32 v35, v137, 1, 3
	s_waitcnt vmcnt(4)
	ds_write_b128 v225, v[20:23] offset:0x4000
	v_lshlrev_b32_e32 v36, 5, v35
	v_add3_u32 v32, v33, s15, v32
	s_movk_i32 s16, 0x60
	ds_write_b128 v226, v[16:19] offset:0x4000
	v_xad_u32 v204, v36, s16, v32
	s_movk_i32 s16, 0x80
	ds_write_b64 v64, v[8:9] offset:0x4000
	v_xad_u32 v205, v36, s16, v32
	s_movk_i32 s16, 0xa0
	ds_write_b64 v65, v[10:11] offset:0x4000
	s_add_u32 s8, s6, 0x100
	v_xad_u32 v206, v36, s16, v32
	s_movk_i32 s16, 0xc0
	ds_write_b64 v66, v[0:1] offset:0x4000
	s_addc_u32 s9, s7, 0
	v_xad_u32 v207, v36, s16, v32
	s_movk_i32 s16, 0xe0
	ds_write_b64 v67, v[2:3] offset:0x4000
	v_add_u32_e32 v201, v32, v36
	v_xad_u32 v202, v36, 32, v32
	v_xad_u32 v203, v36, 64, v32
	v_xad_u32 v208, v36, s16, v32
	v_lshl_add_u32 v32, v143, 7, s10
	s_add_u32 s10, s78, 0x20000
	global_load_dwordx4 v[132:135], v198, s[8:9]
	s_addc_u32 s11, s79, 0
	global_load_dwordx4 v[128:131], v199, s[8:9]
	v_lshrrev_b32_e32 v34, 1, v137
	global_load_dwordx4 v[136:139], v196, s[10:11]
	s_add_u32 s6, s6, 0x180
	v_bitop3_b32 v34, v140, v34, 7 bitop3:0x78
	v_bitop3_b32 v37, v140, v35, 2 bitop3:0x36
	v_bitop3_b32 v38, v140, v35, 4 bitop3:0x36
	v_bitop3_b32 v35, v140, v35, 6 bitop3:0x36
	global_load_dwordx4 v[140:143], v197, s[10:11]
	s_addc_u32 s7, s7, 0
	s_add_u32 s8, s78, 0x30000
	global_load_dwordx4 v[148:151], v198, s[6:7]
	s_addc_u32 s9, s79, 0
	global_load_dwordx4 v[144:147], v199, s[6:7]
	global_load_dwordx4 v[152:155], v196, s[8:9]
	s_add_u32 s10, s13, s14
	global_load_dwordx4 v[156:159], v197, s[8:9]
	s_addc_u32 s11, s12, 0
	s_add_u32 s12, s41, s30
	v_mov_b32_e32 v0, 0
	s_mov_b32 s4, 0
	v_lshl_add_u32 v209, v34, 4, v32
	v_lshl_add_u32 v210, v37, 4, v32
	v_lshl_add_u32 v211, v38, 4, v32
	v_lshl_add_u32 v224, v35, 4, v32
	s_addc_u32 s13, 0, s31
	v_mov_b32_e32 v1, v0
	v_mov_b32_e32 v2, v0
	v_mov_b32_e32 v3, v0
	v_mov_b32_e32 v4, v0
	v_mov_b32_e32 v5, v0
	v_mov_b32_e32 v6, v0
	v_mov_b32_e32 v7, v0
	v_mov_b32_e32 v8, v0
	v_mov_b32_e32 v9, v0
	v_mov_b32_e32 v10, v0
	v_mov_b32_e32 v11, v0
	v_mov_b32_e32 v12, v0
	v_mov_b32_e32 v13, v0
	v_mov_b32_e32 v14, v0
	v_mov_b32_e32 v15, v0
	v_mov_b32_e32 v16, v0
	v_mov_b32_e32 v17, v0
	v_mov_b32_e32 v18, v0
	v_mov_b32_e32 v19, v0
	v_mov_b32_e32 v20, v0
	v_mov_b32_e32 v21, v0
	v_mov_b32_e32 v22, v0
	v_mov_b32_e32 v23, v0
	v_mov_b32_e32 v24, v0
	v_mov_b32_e32 v25, v0
	v_mov_b32_e32 v26, v0
	v_mov_b32_e32 v27, v0
	v_mov_b32_e32 v28, v0
	v_mov_b32_e32 v29, v0
	v_mov_b32_e32 v30, v0
	v_mov_b32_e32 v31, v0
	v_mov_b32_e32 v32, v0
	v_mov_b32_e32 v33, v0
	v_mov_b32_e32 v34, v0
	v_mov_b32_e32 v35, v0
	v_mov_b32_e32 v36, v0
	v_mov_b32_e32 v37, v0
	v_mov_b32_e32 v38, v0
	v_mov_b32_e32 v39, v0
	v_mov_b32_e32 v40, v0
	v_mov_b32_e32 v41, v0
	v_mov_b32_e32 v42, v0
	v_mov_b32_e32 v43, v0
	v_mov_b32_e32 v44, v0
	v_mov_b32_e32 v45, v0
	v_mov_b32_e32 v46, v0
	v_mov_b32_e32 v47, v0
	v_mov_b32_e32 v48, v0
	v_mov_b32_e32 v49, v0
	v_mov_b32_e32 v50, v0
	v_mov_b32_e32 v51, v0
	v_mov_b32_e32 v52, v0
	v_mov_b32_e32 v53, v0
	v_mov_b32_e32 v54, v0
	v_mov_b32_e32 v55, v0
	v_mov_b32_e32 v56, v0
	v_mov_b32_e32 v57, v0
	v_mov_b32_e32 v58, v0
	v_mov_b32_e32 v59, v0
	v_mov_b32_e32 v60, v0
	v_mov_b32_e32 v61, v0
	v_mov_b32_e32 v62, v0
	v_mov_b32_e32 v63, v0
	v_mov_b32_e32 v160, v0
	v_mov_b32_e32 v161, v0
	v_mov_b32_e32 v227, v64
	v_mov_b32_e32 v228, v65
	v_readlane_b32 s100, v250, 8
	v_mbcnt_lo_u32_b32 v68, -1, 0
	v_mbcnt_hi_u32_b32 v68, -1, v68
	v_and_b32_e32 v69, 15, v68
	v_lshrrev_b32_e32 v70, 4, v68
	v_lshlrev_b32_e32 v72, 8, v69
	v_add_u32_e32 v72, 0x10000, v72
	v_add_u32_e32 v71, 0, v70
	v_xor_b32_e32 v71, v71, v69
	v_lshl_add_u32 v201, v71, 4, v72
	v_add_u32_e32 v71, 4, v70
	v_xor_b32_e32 v71, v71, v69
	v_lshl_add_u32 v202, v71, 4, v72
	v_add_u32_e32 v71, 8, v70
	v_xor_b32_e32 v71, v71, v69
	v_lshl_add_u32 v203, v71, 4, v72
	v_add_u32_e32 v71, 12, v70
	v_xor_b32_e32 v71, v71, v69
	v_lshl_add_u32 v204, v71, 4, v72
	v_bfe_u32 v73, v69, 1, 3
	v_lshlrev_b32_e32 v76, 7, v69
	v_add_u32_e32 v71, 0, v70
	v_xor_b32_e32 v71, v71, v73
	v_lshl_add_u32 v209, v71, 4, v76
	v_add_u32_e32 v71, 4, v70
	v_xor_b32_e32 v71, v71, v73
	v_lshl_add_u32 v210, v71, 4, v76
	s_lshl_b32 s101, s100, 7
	s_add_u32 s101, s101, 0x8000
	s_cmpk_ge_u32 s100, 0x100
	s_cselect_b32 s6, 0x8000, 0
	s_add_u32 s101, s101, s6
	v_and_b32_e32 v74, 31, v68
	v_lshrrev_b32_e32 v75, 5, v68
	v_lshlrev_b32_e32 v74, 8, v74
	v_lshl_add_u32 v74, v75, 4, v74
	v_add_u32_e32 v74, s101, v74
	v_lshlrev_b32_e32 v75, 8, v69
	v_lshl_add_u32 v75, v70, 4, v75
	v_add_u32_e32 v75, s101, v75
	ds_write_b128 v74, v[96:99] offset:0
	ds_write_b128 v74, v[100:103] offset:32
	ds_write_b128 v74, v[104:107] offset:64
	ds_write_b128 v74, v[108:111] offset:96
	ds_write_b128 v74, v[112:115] offset:128
	ds_write_b128 v74, v[116:119] offset:160
	ds_write_b128 v74, v[120:123] offset:192
	ds_write_b128 v74, v[124:127] offset:224
	s_waitcnt lgkmcnt(0)
	ds_read_b128 v[96:99], v75 offset:0
	ds_read_b128 v[100:103], v75 offset:64
	ds_read_b128 v[104:107], v75 offset:128
	ds_read_b128 v[108:111], v75 offset:192
	ds_read_b128 v[112:115], v75 offset:4096
	ds_read_b128 v[116:119], v75 offset:4160
	ds_read_b128 v[120:123], v75 offset:4224
	ds_read_b128 v[124:127], v75 offset:4288
	v_mov_b32_e32 v76, 0
	v_mov_b32_e32 v77, 0
	v_mov_b32_e32 v78, 0
	v_mov_b32_e32 v79, 0
	s_lshl_b32 s6, s100, 5
	s_add_u32 s6, s6, 0x24000
	v_lshlrev_b32_e32 v71, 4, v68
	v_add_u32_e32 v71, s6, v71
	ds_write_b128 v71, v[76:79] offset:0
	ds_write_b128 v71, v[76:79] offset:1024
	s_waitcnt lgkmcnt(0)
	s_barrier
	v_mov_b32_e32 v194, 0
	v_mov_b32_e32 v195, 0
	v_mov_b32_e32 v64, 0
	v_mov_b32_e32 v65, 0
	v_mov_b32_e32 v66, 0
	v_mov_b32_e32 v67, 0
	v_mov_b32_e32 v68, 0
	v_mov_b32_e32 v69, 0
	v_mov_b32_e32 v70, 0
	v_mov_b32_e32 v71, 0
	v_mov_b32_e32 v72, 0xff800000
	v_mov_b32_e32 v80, v72
	v_mov_b32_e32 v81, v72
	v_mov_b32_e32 v82, v72
	v_mov_b32_e32 v83, v72
	v_mov_b32_e32 v84, v72
	v_mov_b32_e32 v85, v72
	v_mov_b32_e32 v86, v72
	v_mov_b32_e32 v87, v72
	v_mov_b32_e32 v88, v72
	v_mov_b32_e32 v89, v72
	v_mov_b32_e32 v90, v72
	v_mov_b32_e32 v91, v72
	v_mov_b32_e32 v92, v72
	v_mov_b32_e32 v93, v72
	v_mov_b32_e32 v94, v72
	v_mov_b32_e32 v95, v72
	s_mov_b32 s6, s100
	s_mov_b32 s100, 0x24000
	s_mov_b32 s101, 0x4000
	v_add_u32_e32 v211, 0x24000, v209
	v_add_u32_e32 v224, 0x24000, v210
	s_cmpk_ge_u32 s6, 0x100
	s_cbranch_scc1 .Lattn_L_entry
.LBB0_734:
	s_barrier
	ds_read_b128 v[160:163], v201 offset:0
	ds_read_b128 v[164:167], v202 offset:0
	ds_read_b128 v[168:171], v203 offset:0
	ds_read_b128 v[172:175], v204 offset:0
	ds_read_b128 v[176:179], v201 offset:4096
	ds_read_b128 v[180:183], v202 offset:4096
	ds_read_b128 v[230:233], v203 offset:4096
	ds_read_b128 v[234:237], v204 offset:4096
	s_waitcnt lgkmcnt(7)
	v_mfma_f32_16x16x32_bf16 v[64:67], v[160:163], v[96:99], 0
	s_waitcnt lgkmcnt(6)
	v_mfma_f32_16x16x32_bf16 v[64:67], v[164:167], v[100:103], v[64:67]
	s_add_u32 s100, s100, 0x4000
	s_cmp_eq_u32 s100, 0x10000
	s_cselect_b32 s100, 0x24000, s100
	s_cmp_eq_u32 s100, 0x28000
	s_cselect_b32 s100, 0, s100
	s_add_u32 s101, s101, 0x4000
	s_cmp_eq_u32 s101, 0x10000
	s_cselect_b32 s101, 0x24000, s101
	s_cmp_eq_u32 s101, 0x28000
	s_cselect_b32 s101, 0, s101
	v_add_u32_e32 v211, s100, v209
	v_add_u32_e32 v224, s100, v210
	v_add_u32_e32 v229, s101, v227
	v_add_u32_e32 v184, s101, v228
	s_add_u32 s16, s22, s10
	s_addc_u32 s17, s23, s11
	s_add_u32 s15, s22, s12
	s_addc_u32 s14, s23, s13
	s_add_u32 s8, s16, 0x3bc00200
	s_addc_u32 s9, s17, 0
	s_add_u32 s6, s15, 0x23a40000
	s_addc_u32 s7, s14, 0
	s_waitcnt lgkmcnt(5)
	v_mfma_f32_16x16x32_bf16 v[64:67], v[168:171], v[104:107], v[64:67]
	s_waitcnt lgkmcnt(4)
	v_mfma_f32_16x16x32_bf16 v[64:67], v[172:175], v[108:111], v[64:67]
	s_waitcnt vmcnt(4)
	ds_write_b128 v225, v[136:139] offset:32768
	v_mfma_f32_16x16x32_bf16 v[68:71], v[172:175], v[124:127], 0
	ds_read_b128 v[172:175], v204 offset:8192
	v_mfma_f32_16x16x32_bf16 v[68:71], v[168:171], v[120:123], v[68:71]
	ds_read_b128 v[168:171], v203 offset:8192
	ds_write_b128 v226, v[140:143] offset:32768
	v_mfma_f32_16x16x32_bf16 v[68:71], v[164:167], v[116:119], v[68:71]
	ds_read_b128 v[164:167], v202 offset:8192
	v_mfma_f32_16x16x32_bf16 v[68:71], v[160:163], v[112:115], v[68:71]
	ds_read_b128 v[160:163], v201 offset:8192
	ds_write_b64 v229, v[132:133] offset:0
	s_waitcnt lgkmcnt(10)
	v_mfma_f32_16x16x32_bf16 v[72:75], v[176:179], v[96:99], 0
	s_waitcnt lgkmcnt(9)
	v_mfma_f32_16x16x32_bf16 v[72:75], v[180:183], v[100:103], v[72:75]
	ds_write_b64 v184, v[134:135] offset:0
	s_waitcnt lgkmcnt(9)
	v_mfma_f32_16x16x32_bf16 v[72:75], v[230:233], v[104:107], v[72:75]
	s_waitcnt lgkmcnt(8)
	v_mfma_f32_16x16x32_bf16 v[72:75], v[234:237], v[108:111], v[72:75]
	ds_write_b64 v229, v[128:129] offset:8192
	v_mfma_f32_16x16x32_bf16 v[76:79], v[234:237], v[124:127], 0
	ds_read_b128 v[234:237], v204 offset:12288
	v_mfma_f32_16x16x32_bf16 v[76:79], v[230:233], v[120:123], v[76:79]
	ds_read_b128 v[230:233], v203 offset:12288
	ds_write_b64 v184, v[130:131] offset:8192
	v_mfma_f32_16x16x32_bf16 v[76:79], v[180:183], v[116:119], v[76:79]
	ds_read_b128 v[180:183], v202 offset:12288
	v_mfma_f32_16x16x32_bf16 v[76:79], v[176:179], v[112:115], v[76:79]
	ds_read_b128 v[176:179], v201 offset:12288
	global_load_dwordx4 v[132:135], v198, s[8:9]
	s_waitcnt lgkmcnt(8)
	v_mfma_f32_16x16x32_bf16 v[80:83], v[160:163], v[96:99], 0
	v_exp_f32_e32 v64, v64
	v_exp_f32_e32 v65, v65
	v_exp_f32_e32 v66, v66
	v_mfma_f32_16x16x32_bf16 v[80:83], v[164:167], v[100:103], v[80:83]
	v_exp_f32_e32 v67, v67
	v_exp_f32_e32 v68, v68
	v_exp_f32_e32 v69, v69
	global_load_dwordx4 v[128:131], v199, s[8:9]
	v_mfma_f32_16x16x32_bf16 v[80:83], v[168:171], v[104:107], v[80:83]
	v_exp_f32_e32 v70, v70
	v_exp_f32_e32 v71, v71
	v_add_f32_e32 v194, v194, v64
	v_mfma_f32_16x16x32_bf16 v[80:83], v[172:175], v[108:111], v[80:83]
	v_add_f32_e32 v194, v194, v65
	v_add_f32_e32 v194, v194, v66
	v_add_f32_e32 v194, v194, v67
	global_load_dwordx4 v[136:139], v196, s[6:7]
	v_mfma_f32_16x16x32_bf16 v[84:87], v[172:175], v[124:127], 0
	v_add_f32_e32 v195, v195, v68
	v_add_f32_e32 v195, v195, v69
	v_add_f32_e32 v195, v195, v70
	ds_read_b128 v[172:175], v211 offset:6144
	v_mfma_f32_16x16x32_bf16 v[84:87], v[168:171], v[120:123], v[84:87]
	v_add_f32_e32 v195, v195, v71
	v_cvt_pk_bf16_f32 v64, v64, v65
	v_cvt_pk_bf16_f32 v65, v66, v67
	ds_read_b128 v[168:171], v211 offset:4096
	global_load_dwordx4 v[140:143], v197, s[6:7]
	v_mfma_f32_16x16x32_bf16 v[84:87], v[164:167], v[116:119], v[84:87]
	v_cvt_pk_bf16_f32 v68, v68, v69
	v_cvt_pk_bf16_f32 v69, v70, v71
	ds_read_b128 v[164:167], v211 offset:2048
	v_mfma_f32_16x16x32_bf16 v[84:87], v[160:163], v[112:115], v[84:87]
	ds_read_b128 v[160:163], v211 offset:0
	s_waitcnt lgkmcnt(4)
	v_mfma_f32_16x16x32_bf16 v[88:91], v[176:179], v[96:99], 0
	v_exp_f32_e32 v72, v72
	v_exp_f32_e32 v73, v73
	v_exp_f32_e32 v74, v74
	v_mfma_f32_16x16x32_bf16 v[88:91], v[180:183], v[100:103], v[88:91]
	v_exp_f32_e32 v75, v75
	v_exp_f32_e32 v76, v76
	v_exp_f32_e32 v77, v77
	v_mfma_f32_16x16x32_bf16 v[88:91], v[230:233], v[104:107], v[88:91]
	v_exp_f32_e32 v78, v78
	v_exp_f32_e32 v79, v79
	v_add_f32_e32 v194, v194, v72
	v_mfma_f32_16x16x32_bf16 v[88:91], v[234:237], v[108:111], v[88:91]
	v_add_f32_e32 v194, v194, v73
	v_add_f32_e32 v194, v194, v74
	v_add_f32_e32 v194, v194, v75
	v_mfma_f32_16x16x32_bf16 v[92:95], v[234:237], v[124:127], 0
	v_add_f32_e32 v195, v195, v76
	v_add_f32_e32 v195, v195, v77
	v_add_f32_e32 v195, v195, v78
	ds_read_b128 v[234:237], v211 offset:14336
	v_mfma_f32_16x16x32_bf16 v[92:95], v[230:233], v[120:123], v[92:95]
	v_add_f32_e32 v195, v195, v79
	v_cvt_pk_bf16_f32 v66, v72, v73
	v_cvt_pk_bf16_f32 v67, v74, v75
	ds_read_b128 v[230:233], v211 offset:12288
	v_mfma_f32_16x16x32_bf16 v[92:95], v[180:183], v[116:119], v[92:95]
	v_cvt_pk_bf16_f32 v70, v76, v77
	v_cvt_pk_bf16_f32 v71, v78, v79
	ds_read_b128 v[180:183], v211 offset:10240
	v_mfma_f32_16x16x32_bf16 v[92:95], v[176:179], v[112:115], v[92:95]
	ds_read_b128 v[176:179], v211 offset:8192
	s_waitcnt lgkmcnt(4)
	v_mfma_f32_16x16x32_bf16 v[0:3], v[160:163], v[64:67], v[0:3]
	v_exp_f32_e32 v80, v80
	v_exp_f32_e32 v81, v81
	v_exp_f32_e32 v82, v82
	v_mfma_f32_16x16x32_bf16 v[4:7], v[160:163], v[68:71], v[4:7]
	v_exp_f32_e32 v83, v83
	v_exp_f32_e32 v84, v84
	v_exp_f32_e32 v85, v85
	ds_read_b128 v[160:163], v224 offset:0
	v_mfma_f32_16x16x32_bf16 v[12:15], v[164:167], v[68:71], v[12:15]
	v_exp_f32_e32 v86, v86
	v_exp_f32_e32 v87, v87
	v_add_f32_e32 v194, v194, v80
	v_mfma_f32_16x16x32_bf16 v[8:11], v[164:167], v[64:67], v[8:11]
	v_add_f32_e32 v194, v194, v81
	v_add_f32_e32 v194, v194, v82
	v_add_f32_e32 v194, v194, v83
	ds_read_b128 v[164:167], v224 offset:2048
	v_mfma_f32_16x16x32_bf16 v[16:19], v[168:171], v[64:67], v[16:19]
	v_add_f32_e32 v195, v195, v84
	v_add_f32_e32 v195, v195, v85
	v_add_f32_e32 v195, v195, v86
	v_mfma_f32_16x16x32_bf16 v[20:23], v[168:171], v[68:71], v[20:23]
	v_add_f32_e32 v195, v195, v87
	v_cvt_pk_bf16_f32 v80, v80, v81
	v_cvt_pk_bf16_f32 v81, v82, v83
	ds_read_b128 v[168:171], v224 offset:4096
	v_mfma_f32_16x16x32_bf16 v[28:31], v[172:175], v[68:71], v[28:31]
	v_cvt_pk_bf16_f32 v84, v84, v85
	v_cvt_pk_bf16_f32 v85, v86, v87
	v_mfma_f32_16x16x32_bf16 v[24:27], v[172:175], v[64:67], v[24:27]
	ds_read_b128 v[172:175], v224 offset:6144
	s_waitcnt lgkmcnt(4)
	v_mfma_f32_16x16x32_bf16 v[32:35], v[176:179], v[64:67], v[32:35]
	v_exp_f32_e32 v88, v88
	v_exp_f32_e32 v89, v89
	v_exp_f32_e32 v90, v90
	v_mfma_f32_16x16x32_bf16 v[36:39], v[176:179], v[68:71], v[36:39]
	v_exp_f32_e32 v91, v91
	v_exp_f32_e32 v92, v92
	v_exp_f32_e32 v93, v93
	ds_read_b128 v[176:179], v224 offset:8192
	v_mfma_f32_16x16x32_bf16 v[44:47], v[180:183], v[68:71], v[44:47]
	v_exp_f32_e32 v94, v94
	v_exp_f32_e32 v95, v95
	v_add_f32_e32 v194, v194, v88
	v_mfma_f32_16x16x32_bf16 v[40:43], v[180:183], v[64:67], v[40:43]
	v_add_f32_e32 v194, v194, v89
	v_add_f32_e32 v194, v194, v90
	v_add_f32_e32 v194, v194, v91
	ds_read_b128 v[180:183], v224 offset:10240
	v_mfma_f32_16x16x32_bf16 v[48:51], v[230:233], v[64:67], v[48:51]
	v_add_f32_e32 v195, v195, v92
	v_add_f32_e32 v195, v195, v93
	v_add_f32_e32 v195, v195, v94
	v_mfma_f32_16x16x32_bf16 v[52:55], v[230:233], v[68:71], v[52:55]
	v_add_f32_e32 v195, v195, v95
	v_cvt_pk_bf16_f32 v82, v88, v89
	v_cvt_pk_bf16_f32 v83, v90, v91
	ds_read_b128 v[230:233], v224 offset:12288
	v_mfma_f32_16x16x32_bf16 v[60:63], v[234:237], v[68:71], v[60:63]
	v_cvt_pk_bf16_f32 v86, v92, v93
	v_cvt_pk_bf16_f32 v87, v94, v95
	v_mfma_f32_16x16x32_bf16 v[56:59], v[234:237], v[64:67], v[56:59]
	ds_read_b128 v[234:237], v224 offset:14336
	s_waitcnt lgkmcnt(7)
	v_mfma_f32_16x16x32_bf16 v[0:3], v[160:163], v[80:83], v[0:3]
	v_mfma_f32_16x16x32_bf16 v[4:7], v[160:163], v[84:87], v[4:7]
	ds_read_b128 v[160:163], v201 offset:16384
	s_waitcnt lgkmcnt(7)
	v_mfma_f32_16x16x32_bf16 v[12:15], v[164:167], v[84:87], v[12:15]
	v_mfma_f32_16x16x32_bf16 v[8:11], v[164:167], v[80:83], v[8:11]
	ds_read_b128 v[164:167], v202 offset:16384
	s_waitcnt lgkmcnt(7)
	v_mfma_f32_16x16x32_bf16 v[16:19], v[168:171], v[80:83], v[16:19]
	v_mfma_f32_16x16x32_bf16 v[20:23], v[168:171], v[84:87], v[20:23]
	ds_read_b128 v[168:171], v203 offset:16384
	s_waitcnt lgkmcnt(7)
	v_mfma_f32_16x16x32_bf16 v[28:31], v[172:175], v[84:87], v[28:31]
	v_mfma_f32_16x16x32_bf16 v[24:27], v[172:175], v[80:83], v[24:27]
	ds_read_b128 v[172:175], v204 offset:16384
	s_waitcnt lgkmcnt(7)
	v_mfma_f32_16x16x32_bf16 v[32:35], v[176:179], v[80:83], v[32:35]
	v_mfma_f32_16x16x32_bf16 v[36:39], v[176:179], v[84:87], v[36:39]
	ds_read_b128 v[176:179], v201 offset:20480
	s_waitcnt lgkmcnt(7)
	v_mfma_f32_16x16x32_bf16 v[44:47], v[180:183], v[84:87], v[44:47]
	v_mfma_f32_16x16x32_bf16 v[40:43], v[180:183], v[80:83], v[40:43]
	ds_read_b128 v[180:183], v202 offset:20480
	s_waitcnt lgkmcnt(7)
	v_mfma_f32_16x16x32_bf16 v[48:51], v[230:233], v[80:83], v[48:51]
	v_mfma_f32_16x16x32_bf16 v[52:55], v[230:233], v[84:87], v[52:55]
	ds_read_b128 v[230:233], v203 offset:20480
	s_waitcnt lgkmcnt(7)
	v_mfma_f32_16x16x32_bf16 v[60:63], v[234:237], v[84:87], v[60:63]
	v_mfma_f32_16x16x32_bf16 v[56:59], v[234:237], v[80:83], v[56:59]
	ds_read_b128 v[234:237], v204 offset:20480
	s_waitcnt lgkmcnt(7)
	v_mfma_f32_16x16x32_bf16 v[64:67], v[160:163], v[96:99], 0
	s_waitcnt lgkmcnt(6)
	v_mfma_f32_16x16x32_bf16 v[64:67], v[164:167], v[100:103], v[64:67]
	s_add_u32 s100, s100, 0x4000
	s_cmp_eq_u32 s100, 0x10000
	s_cselect_b32 s100, 0x24000, s100
	s_cmp_eq_u32 s100, 0x28000
	s_cselect_b32 s100, 0, s100
	s_add_u32 s101, s101, 0x4000
	s_cmp_eq_u32 s101, 0x10000
	s_cselect_b32 s101, 0x24000, s101
	s_cmp_eq_u32 s101, 0x28000
	s_cselect_b32 s101, 0, s101
	v_add_u32_e32 v211, s100, v209
	v_add_u32_e32 v224, s100, v210
	v_add_u32_e32 v229, s101, v227
	v_add_u32_e32 v184, s101, v228
	s_add_u32 s8, s16, 0x3bc00280
	s_addc_u32 s9, s17, 0
	s_add_u32 s6, s15, 0x23a50000
	s_addc_u32 s7, s14, 0
	s_waitcnt lgkmcnt(5)
	v_mfma_f32_16x16x32_bf16 v[64:67], v[168:171], v[104:107], v[64:67]
	s_waitcnt lgkmcnt(4)
	v_mfma_f32_16x16x32_bf16 v[64:67], v[172:175], v[108:111], v[64:67]
	s_waitcnt vmcnt(4)
	ds_write_b128 v225, v[152:155] offset:49152
	v_mfma_f32_16x16x32_bf16 v[68:71], v[172:175], v[124:127], 0
	ds_read_b128 v[172:175], v204 offset:24576
	v_mfma_f32_16x16x32_bf16 v[68:71], v[168:171], v[120:123], v[68:71]
	ds_read_b128 v[168:171], v203 offset:24576
	ds_write_b128 v226, v[156:159] offset:49152
	v_mfma_f32_16x16x32_bf16 v[68:71], v[164:167], v[116:119], v[68:71]
	ds_read_b128 v[164:167], v202 offset:24576
	v_mfma_f32_16x16x32_bf16 v[68:71], v[160:163], v[112:115], v[68:71]
	ds_read_b128 v[160:163], v201 offset:24576
	ds_write_b64 v229, v[148:149] offset:0
	s_waitcnt lgkmcnt(10)
	v_mfma_f32_16x16x32_bf16 v[72:75], v[176:179], v[96:99], 0
	s_waitcnt lgkmcnt(9)
	v_mfma_f32_16x16x32_bf16 v[72:75], v[180:183], v[100:103], v[72:75]
	ds_write_b64 v184, v[150:151] offset:0
	s_waitcnt lgkmcnt(9)
	v_mfma_f32_16x16x32_bf16 v[72:75], v[230:233], v[104:107], v[72:75]
	s_waitcnt lgkmcnt(8)
	v_mfma_f32_16x16x32_bf16 v[72:75], v[234:237], v[108:111], v[72:75]
	ds_write_b64 v229, v[144:145] offset:8192
	v_mfma_f32_16x16x32_bf16 v[76:79], v[234:237], v[124:127], 0
	ds_read_b128 v[234:237], v204 offset:28672
	v_mfma_f32_16x16x32_bf16 v[76:79], v[230:233], v[120:123], v[76:79]
	ds_read_b128 v[230:233], v203 offset:28672
	ds_write_b64 v184, v[146:147] offset:8192
	v_mfma_f32_16x16x32_bf16 v[76:79], v[180:183], v[116:119], v[76:79]
	ds_read_b128 v[180:183], v202 offset:28672
	v_mfma_f32_16x16x32_bf16 v[76:79], v[176:179], v[112:115], v[76:79]
	ds_read_b128 v[176:179], v201 offset:28672
	global_load_dwordx4 v[148:151], v198, s[8:9]
	s_waitcnt lgkmcnt(8)
	v_mfma_f32_16x16x32_bf16 v[80:83], v[160:163], v[96:99], 0
	v_exp_f32_e32 v64, v64
	v_exp_f32_e32 v65, v65
	v_exp_f32_e32 v66, v66
	v_mfma_f32_16x16x32_bf16 v[80:83], v[164:167], v[100:103], v[80:83]
	v_exp_f32_e32 v67, v67
	v_exp_f32_e32 v68, v68
	v_exp_f32_e32 v69, v69
	global_load_dwordx4 v[144:147], v199, s[8:9]
	v_mfma_f32_16x16x32_bf16 v[80:83], v[168:171], v[104:107], v[80:83]
	v_exp_f32_e32 v70, v70
	v_exp_f32_e32 v71, v71
	v_add_f32_e32 v194, v194, v64
	v_mfma_f32_16x16x32_bf16 v[80:83], v[172:175], v[108:111], v[80:83]
	v_add_f32_e32 v194, v194, v65
	v_add_f32_e32 v194, v194, v66
	v_add_f32_e32 v194, v194, v67
	global_load_dwordx4 v[152:155], v196, s[6:7]
	v_mfma_f32_16x16x32_bf16 v[84:87], v[172:175], v[124:127], 0
	v_add_f32_e32 v195, v195, v68
	v_add_f32_e32 v195, v195, v69
	v_add_f32_e32 v195, v195, v70
	ds_read_b128 v[172:175], v211 offset:6144
	v_mfma_f32_16x16x32_bf16 v[84:87], v[168:171], v[120:123], v[84:87]
	v_add_f32_e32 v195, v195, v71
	v_cvt_pk_bf16_f32 v64, v64, v65
	v_cvt_pk_bf16_f32 v65, v66, v67
	ds_read_b128 v[168:171], v211 offset:4096
	global_load_dwordx4 v[156:159], v197, s[6:7]
	v_mfma_f32_16x16x32_bf16 v[84:87], v[164:167], v[116:119], v[84:87]
	v_cvt_pk_bf16_f32 v68, v68, v69
	v_cvt_pk_bf16_f32 v69, v70, v71
	ds_read_b128 v[164:167], v211 offset:2048
	v_mfma_f32_16x16x32_bf16 v[84:87], v[160:163], v[112:115], v[84:87]
	ds_read_b128 v[160:163], v211 offset:0
	s_waitcnt lgkmcnt(4)
	v_mfma_f32_16x16x32_bf16 v[88:91], v[176:179], v[96:99], 0
	v_exp_f32_e32 v72, v72
	v_exp_f32_e32 v73, v73
	v_exp_f32_e32 v74, v74
	v_mfma_f32_16x16x32_bf16 v[88:91], v[180:183], v[100:103], v[88:91]
	v_exp_f32_e32 v75, v75
	v_exp_f32_e32 v76, v76
	v_exp_f32_e32 v77, v77
	v_mfma_f32_16x16x32_bf16 v[88:91], v[230:233], v[104:107], v[88:91]
	v_exp_f32_e32 v78, v78
	v_exp_f32_e32 v79, v79
	v_add_f32_e32 v194, v194, v72
	v_mfma_f32_16x16x32_bf16 v[88:91], v[234:237], v[108:111], v[88:91]
	v_add_f32_e32 v194, v194, v73
	v_add_f32_e32 v194, v194, v74
	v_add_f32_e32 v194, v194, v75
	v_mfma_f32_16x16x32_bf16 v[92:95], v[234:237], v[124:127], 0
	v_add_f32_e32 v195, v195, v76
	v_add_f32_e32 v195, v195, v77
	v_add_f32_e32 v195, v195, v78
	ds_read_b128 v[234:237], v211 offset:14336
	v_mfma_f32_16x16x32_bf16 v[92:95], v[230:233], v[120:123], v[92:95]
	v_add_f32_e32 v195, v195, v79
	v_cvt_pk_bf16_f32 v66, v72, v73
	v_cvt_pk_bf16_f32 v67, v74, v75
	ds_read_b128 v[230:233], v211 offset:12288
	v_mfma_f32_16x16x32_bf16 v[92:95], v[180:183], v[116:119], v[92:95]
	v_cvt_pk_bf16_f32 v70, v76, v77
	v_cvt_pk_bf16_f32 v71, v78, v79
	ds_read_b128 v[180:183], v211 offset:10240
	v_mfma_f32_16x16x32_bf16 v[92:95], v[176:179], v[112:115], v[92:95]
	ds_read_b128 v[176:179], v211 offset:8192
	s_waitcnt lgkmcnt(4)
	v_mfma_f32_16x16x32_bf16 v[0:3], v[160:163], v[64:67], v[0:3]
	v_exp_f32_e32 v80, v80
	v_exp_f32_e32 v81, v81
	v_exp_f32_e32 v82, v82
	v_mfma_f32_16x16x32_bf16 v[4:7], v[160:163], v[68:71], v[4:7]
	v_exp_f32_e32 v83, v83
	v_exp_f32_e32 v84, v84
	v_exp_f32_e32 v85, v85
	ds_read_b128 v[160:163], v224 offset:0
	v_mfma_f32_16x16x32_bf16 v[12:15], v[164:167], v[68:71], v[12:15]
	v_exp_f32_e32 v86, v86
	v_exp_f32_e32 v87, v87
	v_add_f32_e32 v194, v194, v80
	v_mfma_f32_16x16x32_bf16 v[8:11], v[164:167], v[64:67], v[8:11]
	v_add_f32_e32 v194, v194, v81
	v_add_f32_e32 v194, v194, v82
	v_add_f32_e32 v194, v194, v83
	ds_read_b128 v[164:167], v224 offset:2048
	v_mfma_f32_16x16x32_bf16 v[16:19], v[168:171], v[64:67], v[16:19]
	v_add_f32_e32 v195, v195, v84
	v_add_f32_e32 v195, v195, v85
	v_add_f32_e32 v195, v195, v86
	v_mfma_f32_16x16x32_bf16 v[20:23], v[168:171], v[68:71], v[20:23]
	v_add_f32_e32 v195, v195, v87
	v_cvt_pk_bf16_f32 v80, v80, v81
	v_cvt_pk_bf16_f32 v81, v82, v83
	ds_read_b128 v[168:171], v224 offset:4096
	v_mfma_f32_16x16x32_bf16 v[28:31], v[172:175], v[68:71], v[28:31]
	v_cvt_pk_bf16_f32 v84, v84, v85
	v_cvt_pk_bf16_f32 v85, v86, v87
	v_mfma_f32_16x16x32_bf16 v[24:27], v[172:175], v[64:67], v[24:27]
	ds_read_b128 v[172:175], v224 offset:6144
	s_waitcnt lgkmcnt(4)
	v_mfma_f32_16x16x32_bf16 v[32:35], v[176:179], v[64:67], v[32:35]
	v_exp_f32_e32 v88, v88
	v_exp_f32_e32 v89, v89
	v_exp_f32_e32 v90, v90
	v_mfma_f32_16x16x32_bf16 v[36:39], v[176:179], v[68:71], v[36:39]
	v_exp_f32_e32 v91, v91
	v_exp_f32_e32 v92, v92
	v_exp_f32_e32 v93, v93
	ds_read_b128 v[176:179], v224 offset:8192
	v_mfma_f32_16x16x32_bf16 v[44:47], v[180:183], v[68:71], v[44:47]
	v_exp_f32_e32 v94, v94
	v_exp_f32_e32 v95, v95
	v_add_f32_e32 v194, v194, v88
	v_mfma_f32_16x16x32_bf16 v[40:43], v[180:183], v[64:67], v[40:43]
	v_add_f32_e32 v194, v194, v89
	v_add_f32_e32 v194, v194, v90
	v_add_f32_e32 v194, v194, v91
	ds_read_b128 v[180:183], v224 offset:10240
	v_mfma_f32_16x16x32_bf16 v[48:51], v[230:233], v[64:67], v[48:51]
	v_add_f32_e32 v195, v195, v92
	v_add_f32_e32 v195, v195, v93
	v_add_f32_e32 v195, v195, v94
	v_mfma_f32_16x16x32_bf16 v[52:55], v[230:233], v[68:71], v[52:55]
	v_add_f32_e32 v195, v195, v95
	v_cvt_pk_bf16_f32 v82, v88, v89
	v_cvt_pk_bf16_f32 v83, v90, v91
	ds_read_b128 v[230:233], v224 offset:12288
	v_mfma_f32_16x16x32_bf16 v[60:63], v[234:237], v[68:71], v[60:63]
	v_cvt_pk_bf16_f32 v86, v92, v93
	v_cvt_pk_bf16_f32 v87, v94, v95
	v_mfma_f32_16x16x32_bf16 v[56:59], v[234:237], v[64:67], v[56:59]
	ds_read_b128 v[234:237], v224 offset:14336
	s_waitcnt lgkmcnt(7)
	v_mfma_f32_16x16x32_bf16 v[0:3], v[160:163], v[80:83], v[0:3]
	v_mfma_f32_16x16x32_bf16 v[4:7], v[160:163], v[84:87], v[4:7]
	s_waitcnt lgkmcnt(6)
	v_mfma_f32_16x16x32_bf16 v[12:15], v[164:167], v[84:87], v[12:15]
	v_mfma_f32_16x16x32_bf16 v[8:11], v[164:167], v[80:83], v[8:11]
	s_waitcnt lgkmcnt(5)
	v_mfma_f32_16x16x32_bf16 v[16:19], v[168:171], v[80:83], v[16:19]
	v_mfma_f32_16x16x32_bf16 v[20:23], v[168:171], v[84:87], v[20:23]
	s_waitcnt lgkmcnt(4)
	v_mfma_f32_16x16x32_bf16 v[28:31], v[172:175], v[84:87], v[28:31]
	v_mfma_f32_16x16x32_bf16 v[24:27], v[172:175], v[80:83], v[24:27]
	s_waitcnt lgkmcnt(3)
	v_mfma_f32_16x16x32_bf16 v[32:35], v[176:179], v[80:83], v[32:35]
	v_mfma_f32_16x16x32_bf16 v[36:39], v[176:179], v[84:87], v[36:39]
	s_waitcnt lgkmcnt(2)
	v_mfma_f32_16x16x32_bf16 v[44:47], v[180:183], v[84:87], v[44:47]
	v_mfma_f32_16x16x32_bf16 v[40:43], v[180:183], v[80:83], v[40:43]
	s_waitcnt lgkmcnt(1)
	v_mfma_f32_16x16x32_bf16 v[48:51], v[230:233], v[80:83], v[48:51]
	v_mfma_f32_16x16x32_bf16 v[52:55], v[230:233], v[84:87], v[52:55]
	s_waitcnt lgkmcnt(0)
	v_mfma_f32_16x16x32_bf16 v[60:63], v[234:237], v[84:87], v[60:63]
	v_mfma_f32_16x16x32_bf16 v[56:59], v[234:237], v[80:83], v[56:59]
	s_barrier
	ds_read_b128 v[160:163], v201 offset:32768
	ds_read_b128 v[164:167], v202 offset:32768
	ds_read_b128 v[168:171], v203 offset:32768
	ds_read_b128 v[172:175], v204 offset:32768
	ds_read_b128 v[176:179], v201 offset:36864
	ds_read_b128 v[180:183], v202 offset:36864
	ds_read_b128 v[230:233], v203 offset:36864
	ds_read_b128 v[234:237], v204 offset:36864
	s_waitcnt lgkmcnt(7)
	v_mfma_f32_16x16x32_bf16 v[64:67], v[160:163], v[96:99], 0
	s_waitcnt lgkmcnt(6)
	v_mfma_f32_16x16x32_bf16 v[64:67], v[164:167], v[100:103], v[64:67]
	s_add_u32 s100, s100, 0x4000
	s_cmp_eq_u32 s100, 0x10000
	s_cselect_b32 s100, 0x24000, s100
	s_cmp_eq_u32 s100, 0x28000
	s_cselect_b32 s100, 0, s100
	s_add_u32 s101, s101, 0x4000
	s_cmp_eq_u32 s101, 0x10000
	s_cselect_b32 s101, 0x24000, s101
	s_cmp_eq_u32 s101, 0x28000
	s_cselect_b32 s101, 0, s101
	v_add_u32_e32 v211, s100, v209
	v_add_u32_e32 v224, s100, v210
	v_add_u32_e32 v229, s101, v227
	v_add_u32_e32 v184, s101, v228
	s_add_u32 s8, s16, 0x3bc00300
	s_addc_u32 s9, s17, 0
	s_add_u32 s6, s15, 0x23a60000
	s_addc_u32 s7, s14, 0
	s_waitcnt lgkmcnt(5)
	v_mfma_f32_16x16x32_bf16 v[64:67], v[168:171], v[104:107], v[64:67]
	s_waitcnt lgkmcnt(4)
	v_mfma_f32_16x16x32_bf16 v[64:67], v[172:175], v[108:111], v[64:67]
	s_waitcnt vmcnt(4)
	ds_write_b128 v225, v[136:139] offset:0
	v_mfma_f32_16x16x32_bf16 v[68:71], v[172:175], v[124:127], 0
	ds_read_b128 v[172:175], v204 offset:40960
	v_mfma_f32_16x16x32_bf16 v[68:71], v[168:171], v[120:123], v[68:71]
	ds_read_b128 v[168:171], v203 offset:40960
	ds_write_b128 v226, v[140:143] offset:0
	v_mfma_f32_16x16x32_bf16 v[68:71], v[164:167], v[116:119], v[68:71]
	ds_read_b128 v[164:167], v202 offset:40960
	v_mfma_f32_16x16x32_bf16 v[68:71], v[160:163], v[112:115], v[68:71]
	ds_read_b128 v[160:163], v201 offset:40960
	ds_write_b64 v229, v[132:133] offset:0
	s_waitcnt lgkmcnt(10)
	v_mfma_f32_16x16x32_bf16 v[72:75], v[176:179], v[96:99], 0
	s_waitcnt lgkmcnt(9)
	v_mfma_f32_16x16x32_bf16 v[72:75], v[180:183], v[100:103], v[72:75]
	ds_write_b64 v184, v[134:135] offset:0
	s_waitcnt lgkmcnt(9)
	v_mfma_f32_16x16x32_bf16 v[72:75], v[230:233], v[104:107], v[72:75]
	s_waitcnt lgkmcnt(8)
	v_mfma_f32_16x16x32_bf16 v[72:75], v[234:237], v[108:111], v[72:75]
	ds_write_b64 v229, v[128:129] offset:8192
	v_mfma_f32_16x16x32_bf16 v[76:79], v[234:237], v[124:127], 0
	ds_read_b128 v[234:237], v204 offset:45056
	v_mfma_f32_16x16x32_bf16 v[76:79], v[230:233], v[120:123], v[76:79]
	ds_read_b128 v[230:233], v203 offset:45056
	ds_write_b64 v184, v[130:131] offset:8192
	v_mfma_f32_16x16x32_bf16 v[76:79], v[180:183], v[116:119], v[76:79]
	ds_read_b128 v[180:183], v202 offset:45056
	v_mfma_f32_16x16x32_bf16 v[76:79], v[176:179], v[112:115], v[76:79]
	ds_read_b128 v[176:179], v201 offset:45056
	global_load_dwordx4 v[132:135], v198, s[8:9]
	s_waitcnt lgkmcnt(8)
	v_mfma_f32_16x16x32_bf16 v[80:83], v[160:163], v[96:99], 0
	v_exp_f32_e32 v64, v64
	v_exp_f32_e32 v65, v65
	v_exp_f32_e32 v66, v66
	v_mfma_f32_16x16x32_bf16 v[80:83], v[164:167], v[100:103], v[80:83]
	v_exp_f32_e32 v67, v67
	v_exp_f32_e32 v68, v68
	v_exp_f32_e32 v69, v69
	global_load_dwordx4 v[128:131], v199, s[8:9]
	v_mfma_f32_16x16x32_bf16 v[80:83], v[168:171], v[104:107], v[80:83]
	v_exp_f32_e32 v70, v70
	v_exp_f32_e32 v71, v71
	v_add_f32_e32 v194, v194, v64
	v_mfma_f32_16x16x32_bf16 v[80:83], v[172:175], v[108:111], v[80:83]
	v_add_f32_e32 v194, v194, v65
	v_add_f32_e32 v194, v194, v66
	v_add_f32_e32 v194, v194, v67
	global_load_dwordx4 v[136:139], v196, s[6:7]
	v_mfma_f32_16x16x32_bf16 v[84:87], v[172:175], v[124:127], 0
	v_add_f32_e32 v195, v195, v68
	v_add_f32_e32 v195, v195, v69
	v_add_f32_e32 v195, v195, v70
	ds_read_b128 v[172:175], v211 offset:6144
	v_mfma_f32_16x16x32_bf16 v[84:87], v[168:171], v[120:123], v[84:87]
	v_add_f32_e32 v195, v195, v71
	v_cvt_pk_bf16_f32 v64, v64, v65
	v_cvt_pk_bf16_f32 v65, v66, v67
	ds_read_b128 v[168:171], v211 offset:4096
	global_load_dwordx4 v[140:143], v197, s[6:7]
	v_mfma_f32_16x16x32_bf16 v[84:87], v[164:167], v[116:119], v[84:87]
	v_cvt_pk_bf16_f32 v68, v68, v69
	v_cvt_pk_bf16_f32 v69, v70, v71
	ds_read_b128 v[164:167], v211 offset:2048
	v_mfma_f32_16x16x32_bf16 v[84:87], v[160:163], v[112:115], v[84:87]
	ds_read_b128 v[160:163], v211 offset:0
	s_waitcnt lgkmcnt(4)
	v_mfma_f32_16x16x32_bf16 v[88:91], v[176:179], v[96:99], 0
	v_exp_f32_e32 v72, v72
	v_exp_f32_e32 v73, v73
	v_exp_f32_e32 v74, v74
	v_mfma_f32_16x16x32_bf16 v[88:91], v[180:183], v[100:103], v[88:91]
	v_exp_f32_e32 v75, v75
	v_exp_f32_e32 v76, v76
	v_exp_f32_e32 v77, v77
	v_mfma_f32_16x16x32_bf16 v[88:91], v[230:233], v[104:107], v[88:91]
	v_exp_f32_e32 v78, v78
	v_exp_f32_e32 v79, v79
	v_add_f32_e32 v194, v194, v72
	v_mfma_f32_16x16x32_bf16 v[88:91], v[234:237], v[108:111], v[88:91]
	v_add_f32_e32 v194, v194, v73
	v_add_f32_e32 v194, v194, v74
	v_add_f32_e32 v194, v194, v75
	v_mfma_f32_16x16x32_bf16 v[92:95], v[234:237], v[124:127], 0
	v_add_f32_e32 v195, v195, v76
	v_add_f32_e32 v195, v195, v77
	v_add_f32_e32 v195, v195, v78
	ds_read_b128 v[234:237], v211 offset:14336
	v_mfma_f32_16x16x32_bf16 v[92:95], v[230:233], v[120:123], v[92:95]
	v_add_f32_e32 v195, v195, v79
	v_cvt_pk_bf16_f32 v66, v72, v73
	v_cvt_pk_bf16_f32 v67, v74, v75
	ds_read_b128 v[230:233], v211 offset:12288
	v_mfma_f32_16x16x32_bf16 v[92:95], v[180:183], v[116:119], v[92:95]
	v_cvt_pk_bf16_f32 v70, v76, v77
	v_cvt_pk_bf16_f32 v71, v78, v79
	ds_read_b128 v[180:183], v211 offset:10240
	v_mfma_f32_16x16x32_bf16 v[92:95], v[176:179], v[112:115], v[92:95]
	ds_read_b128 v[176:179], v211 offset:8192
	s_waitcnt lgkmcnt(4)
	v_mfma_f32_16x16x32_bf16 v[0:3], v[160:163], v[64:67], v[0:3]
	v_exp_f32_e32 v80, v80
	v_exp_f32_e32 v81, v81
	v_exp_f32_e32 v82, v82
	v_mfma_f32_16x16x32_bf16 v[4:7], v[160:163], v[68:71], v[4:7]
	v_exp_f32_e32 v83, v83
	v_exp_f32_e32 v84, v84
	v_exp_f32_e32 v85, v85
	ds_read_b128 v[160:163], v224 offset:0
	v_mfma_f32_16x16x32_bf16 v[12:15], v[164:167], v[68:71], v[12:15]
	v_exp_f32_e32 v86, v86
	v_exp_f32_e32 v87, v87
	v_add_f32_e32 v194, v194, v80
	v_mfma_f32_16x16x32_bf16 v[8:11], v[164:167], v[64:67], v[8:11]
	v_add_f32_e32 v194, v194, v81
	v_add_f32_e32 v194, v194, v82
	v_add_f32_e32 v194, v194, v83
	ds_read_b128 v[164:167], v224 offset:2048
	v_mfma_f32_16x16x32_bf16 v[16:19], v[168:171], v[64:67], v[16:19]
	v_add_f32_e32 v195, v195, v84
	v_add_f32_e32 v195, v195, v85
	v_add_f32_e32 v195, v195, v86
	v_mfma_f32_16x16x32_bf16 v[20:23], v[168:171], v[68:71], v[20:23]
	v_add_f32_e32 v195, v195, v87
	v_cvt_pk_bf16_f32 v80, v80, v81
	v_cvt_pk_bf16_f32 v81, v82, v83
	ds_read_b128 v[168:171], v224 offset:4096
	v_mfma_f32_16x16x32_bf16 v[28:31], v[172:175], v[68:71], v[28:31]
	v_cvt_pk_bf16_f32 v84, v84, v85
	v_cvt_pk_bf16_f32 v85, v86, v87
	v_mfma_f32_16x16x32_bf16 v[24:27], v[172:175], v[64:67], v[24:27]
	ds_read_b128 v[172:175], v224 offset:6144
	s_waitcnt lgkmcnt(4)
	v_mfma_f32_16x16x32_bf16 v[32:35], v[176:179], v[64:67], v[32:35]
	v_exp_f32_e32 v88, v88
	v_exp_f32_e32 v89, v89
	v_exp_f32_e32 v90, v90
	v_mfma_f32_16x16x32_bf16 v[36:39], v[176:179], v[68:71], v[36:39]
	v_exp_f32_e32 v91, v91
	v_exp_f32_e32 v92, v92
	v_exp_f32_e32 v93, v93
	ds_read_b128 v[176:179], v224 offset:8192
	v_mfma_f32_16x16x32_bf16 v[44:47], v[180:183], v[68:71], v[44:47]
	v_exp_f32_e32 v94, v94
	v_exp_f32_e32 v95, v95
	v_add_f32_e32 v194, v194, v88
	v_mfma_f32_16x16x32_bf16 v[40:43], v[180:183], v[64:67], v[40:43]
	v_add_f32_e32 v194, v194, v89
	v_add_f32_e32 v194, v194, v90
	v_add_f32_e32 v194, v194, v91
	ds_read_b128 v[180:183], v224 offset:10240
	v_mfma_f32_16x16x32_bf16 v[48:51], v[230:233], v[64:67], v[48:51]
	v_add_f32_e32 v195, v195, v92
	v_add_f32_e32 v195, v195, v93
	v_add_f32_e32 v195, v195, v94
	v_mfma_f32_16x16x32_bf16 v[52:55], v[230:233], v[68:71], v[52:55]
	v_add_f32_e32 v195, v195, v95
	v_cvt_pk_bf16_f32 v82, v88, v89
	v_cvt_pk_bf16_f32 v83, v90, v91
	ds_read_b128 v[230:233], v224 offset:12288
	v_mfma_f32_16x16x32_bf16 v[60:63], v[234:237], v[68:71], v[60:63]
	v_cvt_pk_bf16_f32 v86, v92, v93
	v_cvt_pk_bf16_f32 v87, v94, v95
	v_mfma_f32_16x16x32_bf16 v[56:59], v[234:237], v[64:67], v[56:59]
	ds_read_b128 v[234:237], v224 offset:14336
	s_waitcnt lgkmcnt(7)
	v_mfma_f32_16x16x32_bf16 v[0:3], v[160:163], v[80:83], v[0:3]
	v_mfma_f32_16x16x32_bf16 v[4:7], v[160:163], v[84:87], v[4:7]
	ds_read_b128 v[160:163], v201 offset:49152
	s_waitcnt lgkmcnt(7)
	v_mfma_f32_16x16x32_bf16 v[12:15], v[164:167], v[84:87], v[12:15]
	v_mfma_f32_16x16x32_bf16 v[8:11], v[164:167], v[80:83], v[8:11]
	ds_read_b128 v[164:167], v202 offset:49152
	s_waitcnt lgkmcnt(7)
	v_mfma_f32_16x16x32_bf16 v[16:19], v[168:171], v[80:83], v[16:19]
	v_mfma_f32_16x16x32_bf16 v[20:23], v[168:171], v[84:87], v[20:23]
	ds_read_b128 v[168:171], v203 offset:49152
	s_waitcnt lgkmcnt(7)
	v_mfma_f32_16x16x32_bf16 v[28:31], v[172:175], v[84:87], v[28:31]
	v_mfma_f32_16x16x32_bf16 v[24:27], v[172:175], v[80:83], v[24:27]
	ds_read_b128 v[172:175], v204 offset:49152
	s_waitcnt lgkmcnt(7)
	v_mfma_f32_16x16x32_bf16 v[32:35], v[176:179], v[80:83], v[32:35]
	v_mfma_f32_16x16x32_bf16 v[36:39], v[176:179], v[84:87], v[36:39]
	ds_read_b128 v[176:179], v201 offset:53248
	s_waitcnt lgkmcnt(7)
	v_mfma_f32_16x16x32_bf16 v[44:47], v[180:183], v[84:87], v[44:47]
	v_mfma_f32_16x16x32_bf16 v[40:43], v[180:183], v[80:83], v[40:43]
	ds_read_b128 v[180:183], v202 offset:53248
	s_waitcnt lgkmcnt(7)
	v_mfma_f32_16x16x32_bf16 v[48:51], v[230:233], v[80:83], v[48:51]
	v_mfma_f32_16x16x32_bf16 v[52:55], v[230:233], v[84:87], v[52:55]
	ds_read_b128 v[230:233], v203 offset:53248
	s_waitcnt lgkmcnt(7)
	v_mfma_f32_16x16x32_bf16 v[60:63], v[234:237], v[84:87], v[60:63]
	v_mfma_f32_16x16x32_bf16 v[56:59], v[234:237], v[80:83], v[56:59]
	ds_read_b128 v[234:237], v204 offset:53248
	s_waitcnt lgkmcnt(7)
	v_mfma_f32_16x16x32_bf16 v[64:67], v[160:163], v[96:99], 0
	s_waitcnt lgkmcnt(6)
	v_mfma_f32_16x16x32_bf16 v[64:67], v[164:167], v[100:103], v[64:67]
	s_add_u32 s100, s100, 0x4000
	s_cmp_eq_u32 s100, 0x10000
	s_cselect_b32 s100, 0x24000, s100
	s_cmp_eq_u32 s100, 0x28000
	s_cselect_b32 s100, 0, s100
	s_add_u32 s101, s101, 0x4000
	s_cmp_eq_u32 s101, 0x10000
	s_cselect_b32 s101, 0x24000, s101
	s_cmp_eq_u32 s101, 0x28000
	s_cselect_b32 s101, 0, s101
	v_add_u32_e32 v211, s100, v209
	v_add_u32_e32 v224, s100, v210
	v_add_u32_e32 v229, s101, v227
	v_add_u32_e32 v184, s101, v228
	s_add_u32 s8, s16, 0x3bc00380
	s_addc_u32 s9, s17, 0
	s_add_u32 s6, s15, 0x23a70000
	s_addc_u32 s7, s14, 0
	s_waitcnt lgkmcnt(5)
	v_mfma_f32_16x16x32_bf16 v[64:67], v[168:171], v[104:107], v[64:67]
	s_waitcnt lgkmcnt(4)
	v_mfma_f32_16x16x32_bf16 v[64:67], v[172:175], v[108:111], v[64:67]
	s_waitcnt vmcnt(4)
	ds_write_b128 v225, v[152:155] offset:16384
	v_mfma_f32_16x16x32_bf16 v[68:71], v[172:175], v[124:127], 0
	ds_read_b128 v[172:175], v204 offset:57344
	v_mfma_f32_16x16x32_bf16 v[68:71], v[168:171], v[120:123], v[68:71]
	ds_read_b128 v[168:171], v203 offset:57344
	ds_write_b128 v226, v[156:159] offset:16384
	v_mfma_f32_16x16x32_bf16 v[68:71], v[164:167], v[116:119], v[68:71]
	ds_read_b128 v[164:167], v202 offset:57344
	v_mfma_f32_16x16x32_bf16 v[68:71], v[160:163], v[112:115], v[68:71]
	ds_read_b128 v[160:163], v201 offset:57344
	ds_write_b64 v229, v[148:149] offset:0
	s_waitcnt lgkmcnt(10)
	v_mfma_f32_16x16x32_bf16 v[72:75], v[176:179], v[96:99], 0
	s_waitcnt lgkmcnt(9)
	v_mfma_f32_16x16x32_bf16 v[72:75], v[180:183], v[100:103], v[72:75]
	ds_write_b64 v184, v[150:151] offset:0
	s_waitcnt lgkmcnt(9)
	v_mfma_f32_16x16x32_bf16 v[72:75], v[230:233], v[104:107], v[72:75]
	s_waitcnt lgkmcnt(8)
	v_mfma_f32_16x16x32_bf16 v[72:75], v[234:237], v[108:111], v[72:75]
	ds_write_b64 v229, v[144:145] offset:8192
	v_mfma_f32_16x16x32_bf16 v[76:79], v[234:237], v[124:127], 0
	ds_read_b128 v[234:237], v204 offset:61440
	v_mfma_f32_16x16x32_bf16 v[76:79], v[230:233], v[120:123], v[76:79]
	ds_read_b128 v[230:233], v203 offset:61440
	ds_write_b64 v184, v[146:147] offset:8192
	v_mfma_f32_16x16x32_bf16 v[76:79], v[180:183], v[116:119], v[76:79]
	ds_read_b128 v[180:183], v202 offset:61440
	v_mfma_f32_16x16x32_bf16 v[76:79], v[176:179], v[112:115], v[76:79]
	ds_read_b128 v[176:179], v201 offset:61440
	global_load_dwordx4 v[148:151], v198, s[8:9]
	s_waitcnt lgkmcnt(8)
	v_mfma_f32_16x16x32_bf16 v[80:83], v[160:163], v[96:99], 0
	v_exp_f32_e32 v64, v64
	v_exp_f32_e32 v65, v65
	v_exp_f32_e32 v66, v66
	v_mfma_f32_16x16x32_bf16 v[80:83], v[164:167], v[100:103], v[80:83]
	v_exp_f32_e32 v67, v67
	v_exp_f32_e32 v68, v68
	v_exp_f32_e32 v69, v69
	global_load_dwordx4 v[144:147], v199, s[8:9]
	v_mfma_f32_16x16x32_bf16 v[80:83], v[168:171], v[104:107], v[80:83]
	v_exp_f32_e32 v70, v70
	v_exp_f32_e32 v71, v71
	v_add_f32_e32 v194, v194, v64
	v_mfma_f32_16x16x32_bf16 v[80:83], v[172:175], v[108:111], v[80:83]
	v_add_f32_e32 v194, v194, v65
	v_add_f32_e32 v194, v194, v66
	v_add_f32_e32 v194, v194, v67
	global_load_dwordx4 v[152:155], v196, s[6:7]
	v_mfma_f32_16x16x32_bf16 v[84:87], v[172:175], v[124:127], 0
	v_add_f32_e32 v195, v195, v68
	v_add_f32_e32 v195, v195, v69
	v_add_f32_e32 v195, v195, v70
	ds_read_b128 v[172:175], v211 offset:6144
	v_mfma_f32_16x16x32_bf16 v[84:87], v[168:171], v[120:123], v[84:87]
	v_add_f32_e32 v195, v195, v71
	v_cvt_pk_bf16_f32 v64, v64, v65
	v_cvt_pk_bf16_f32 v65, v66, v67
	ds_read_b128 v[168:171], v211 offset:4096
	global_load_dwordx4 v[156:159], v197, s[6:7]
	v_mfma_f32_16x16x32_bf16 v[84:87], v[164:167], v[116:119], v[84:87]
	v_cvt_pk_bf16_f32 v68, v68, v69
	v_cvt_pk_bf16_f32 v69, v70, v71
	ds_read_b128 v[164:167], v211 offset:2048
	v_mfma_f32_16x16x32_bf16 v[84:87], v[160:163], v[112:115], v[84:87]
	ds_read_b128 v[160:163], v211 offset:0
	s_waitcnt lgkmcnt(4)
	v_mfma_f32_16x16x32_bf16 v[88:91], v[176:179], v[96:99], 0
	v_exp_f32_e32 v72, v72
	v_exp_f32_e32 v73, v73
	v_exp_f32_e32 v74, v74
	v_mfma_f32_16x16x32_bf16 v[88:91], v[180:183], v[100:103], v[88:91]
	v_exp_f32_e32 v75, v75
	v_exp_f32_e32 v76, v76
	v_exp_f32_e32 v77, v77
	v_mfma_f32_16x16x32_bf16 v[88:91], v[230:233], v[104:107], v[88:91]
	v_exp_f32_e32 v78, v78
	v_exp_f32_e32 v79, v79
	v_add_f32_e32 v194, v194, v72
	v_mfma_f32_16x16x32_bf16 v[88:91], v[234:237], v[108:111], v[88:91]
	v_add_f32_e32 v194, v194, v73
	v_add_f32_e32 v194, v194, v74
	v_add_f32_e32 v194, v194, v75
	v_mfma_f32_16x16x32_bf16 v[92:95], v[234:237], v[124:127], 0
	v_add_f32_e32 v195, v195, v76
	v_add_f32_e32 v195, v195, v77
	v_add_f32_e32 v195, v195, v78
	ds_read_b128 v[234:237], v211 offset:14336
	v_mfma_f32_16x16x32_bf16 v[92:95], v[230:233], v[120:123], v[92:95]
	v_add_f32_e32 v195, v195, v79
	v_cvt_pk_bf16_f32 v66, v72, v73
	v_cvt_pk_bf16_f32 v67, v74, v75
	ds_read_b128 v[230:233], v211 offset:12288
	v_mfma_f32_16x16x32_bf16 v[92:95], v[180:183], v[116:119], v[92:95]
	v_cvt_pk_bf16_f32 v70, v76, v77
	v_cvt_pk_bf16_f32 v71, v78, v79
	ds_read_b128 v[180:183], v211 offset:10240
	v_mfma_f32_16x16x32_bf16 v[92:95], v[176:179], v[112:115], v[92:95]
	ds_read_b128 v[176:179], v211 offset:8192
	s_waitcnt lgkmcnt(4)
	v_mfma_f32_16x16x32_bf16 v[0:3], v[160:163], v[64:67], v[0:3]
	v_exp_f32_e32 v80, v80
	v_exp_f32_e32 v81, v81
	v_exp_f32_e32 v82, v82
	v_mfma_f32_16x16x32_bf16 v[4:7], v[160:163], v[68:71], v[4:7]
	v_exp_f32_e32 v83, v83
	v_exp_f32_e32 v84, v84
	v_exp_f32_e32 v85, v85
	ds_read_b128 v[160:163], v224 offset:0
	v_mfma_f32_16x16x32_bf16 v[12:15], v[164:167], v[68:71], v[12:15]
	v_exp_f32_e32 v86, v86
	v_exp_f32_e32 v87, v87
	v_add_f32_e32 v194, v194, v80
	v_mfma_f32_16x16x32_bf16 v[8:11], v[164:167], v[64:67], v[8:11]
	v_add_f32_e32 v194, v194, v81
	v_add_f32_e32 v194, v194, v82
	v_add_f32_e32 v194, v194, v83
	ds_read_b128 v[164:167], v224 offset:2048
	v_mfma_f32_16x16x32_bf16 v[16:19], v[168:171], v[64:67], v[16:19]
	v_add_f32_e32 v195, v195, v84
	v_add_f32_e32 v195, v195, v85
	v_add_f32_e32 v195, v195, v86
	v_mfma_f32_16x16x32_bf16 v[20:23], v[168:171], v[68:71], v[20:23]
	v_add_f32_e32 v195, v195, v87
	v_cvt_pk_bf16_f32 v80, v80, v81
	v_cvt_pk_bf16_f32 v81, v82, v83
	ds_read_b128 v[168:171], v224 offset:4096
	v_mfma_f32_16x16x32_bf16 v[28:31], v[172:175], v[68:71], v[28:31]
	v_cvt_pk_bf16_f32 v84, v84, v85
	v_cvt_pk_bf16_f32 v85, v86, v87
	v_mfma_f32_16x16x32_bf16 v[24:27], v[172:175], v[64:67], v[24:27]
	ds_read_b128 v[172:175], v224 offset:6144
	s_waitcnt lgkmcnt(4)
	v_mfma_f32_16x16x32_bf16 v[32:35], v[176:179], v[64:67], v[32:35]
	v_exp_f32_e32 v88, v88
	v_exp_f32_e32 v89, v89
	v_exp_f32_e32 v90, v90
	v_mfma_f32_16x16x32_bf16 v[36:39], v[176:179], v[68:71], v[36:39]
	v_exp_f32_e32 v91, v91
	v_exp_f32_e32 v92, v92
	v_exp_f32_e32 v93, v93
	ds_read_b128 v[176:179], v224 offset:8192
	v_mfma_f32_16x16x32_bf16 v[44:47], v[180:183], v[68:71], v[44:47]
	v_exp_f32_e32 v94, v94
	v_exp_f32_e32 v95, v95
	v_add_f32_e32 v194, v194, v88
	v_mfma_f32_16x16x32_bf16 v[40:43], v[180:183], v[64:67], v[40:43]
	v_add_f32_e32 v194, v194, v89
	v_add_f32_e32 v194, v194, v90
	v_add_f32_e32 v194, v194, v91
	ds_read_b128 v[180:183], v224 offset:10240
	v_mfma_f32_16x16x32_bf16 v[48:51], v[230:233], v[64:67], v[48:51]
	v_add_f32_e32 v195, v195, v92
	v_add_f32_e32 v195, v195, v93
	v_add_f32_e32 v195, v195, v94
	v_mfma_f32_16x16x32_bf16 v[52:55], v[230:233], v[68:71], v[52:55]
	v_add_f32_e32 v195, v195, v95
	v_cvt_pk_bf16_f32 v82, v88, v89
	v_cvt_pk_bf16_f32 v83, v90, v91
	ds_read_b128 v[230:233], v224 offset:12288
	v_mfma_f32_16x16x32_bf16 v[60:63], v[234:237], v[68:71], v[60:63]
	v_cvt_pk_bf16_f32 v86, v92, v93
	v_cvt_pk_bf16_f32 v87, v94, v95
	v_mfma_f32_16x16x32_bf16 v[56:59], v[234:237], v[64:67], v[56:59]
	ds_read_b128 v[234:237], v224 offset:14336
	s_waitcnt lgkmcnt(7)
	v_mfma_f32_16x16x32_bf16 v[0:3], v[160:163], v[80:83], v[0:3]
	v_mfma_f32_16x16x32_bf16 v[4:7], v[160:163], v[84:87], v[4:7]
	s_waitcnt lgkmcnt(6)
	v_mfma_f32_16x16x32_bf16 v[12:15], v[164:167], v[84:87], v[12:15]
	v_mfma_f32_16x16x32_bf16 v[8:11], v[164:167], v[80:83], v[8:11]
	s_waitcnt lgkmcnt(5)
	v_mfma_f32_16x16x32_bf16 v[16:19], v[168:171], v[80:83], v[16:19]
	v_mfma_f32_16x16x32_bf16 v[20:23], v[168:171], v[84:87], v[20:23]
	s_waitcnt lgkmcnt(4)
	v_mfma_f32_16x16x32_bf16 v[28:31], v[172:175], v[84:87], v[28:31]
	v_mfma_f32_16x16x32_bf16 v[24:27], v[172:175], v[80:83], v[24:27]
	s_waitcnt lgkmcnt(3)
	v_mfma_f32_16x16x32_bf16 v[32:35], v[176:179], v[80:83], v[32:35]
	v_mfma_f32_16x16x32_bf16 v[36:39], v[176:179], v[84:87], v[36:39]
	s_add_u32 s10, s10, 0x200
	s_addc_u32 s11, s11, 0
	s_add_u32 s12, s12, 0x40000
	s_addc_u32 s13, s13, 0
	s_add_i32 s4, s4, 4
	s_cmpk_lt_u32 s4, 0x104
	s_cselect_b64 s[6:7], -1, 0
	s_and_b64 s[6:7], s[0:1], s[6:7]
	s_and_b64 vcc, exec, s[6:7]
	s_waitcnt lgkmcnt(2)
	v_mfma_f32_16x16x32_bf16 v[44:47], v[180:183], v[84:87], v[44:47]
	v_mfma_f32_16x16x32_bf16 v[40:43], v[180:183], v[80:83], v[40:43]
	s_waitcnt lgkmcnt(1)
	v_mfma_f32_16x16x32_bf16 v[48:51], v[230:233], v[80:83], v[48:51]
	v_mfma_f32_16x16x32_bf16 v[52:55], v[230:233], v[84:87], v[52:55]
	s_waitcnt lgkmcnt(0)
	v_mfma_f32_16x16x32_bf16 v[60:63], v[234:237], v[84:87], v[60:63]
	v_mfma_f32_16x16x32_bf16 v[56:59], v[234:237], v[80:83], v[56:59]
	s_cbranch_vccnz .LBB0_734
	s_branch .Lattn_epi
.Lattn_L_entry:
	ds_read_b128 v[160:163], v211 offset:0
	ds_read_b128 v[164:167], v211 offset:2048
	ds_read_b128 v[168:171], v211 offset:4096
	ds_read_b128 v[172:175], v211 offset:6144
	ds_read_b128 v[176:179], v211 offset:8192
	ds_read_b128 v[180:183], v211 offset:10240
	ds_read_b128 v[230:233], v211 offset:12288
	ds_read_b128 v[234:237], v211 offset:14336
.Lattn_L_top:
	s_barrier
	s_waitcnt lgkmcnt(4)
	v_mfma_f32_16x16x32_bf16 v[0:3], v[160:163], v[64:67], v[0:3]
	v_exp_f32_e32 v80, v80
	v_exp_f32_e32 v81, v81
	v_exp_f32_e32 v82, v82
	v_mfma_f32_16x16x32_bf16 v[4:7], v[160:163], v[68:71], v[4:7]
	v_exp_f32_e32 v83, v83
	v_exp_f32_e32 v84, v84
	v_exp_f32_e32 v85, v85
	ds_read_b128 v[160:163], v224 offset:0
	v_mfma_f32_16x16x32_bf16 v[12:15], v[164:167], v[68:71], v[12:15]
	v_exp_f32_e32 v86, v86
	v_exp_f32_e32 v87, v87
	v_add_f32_e32 v194, v194, v80
	v_mfma_f32_16x16x32_bf16 v[8:11], v[164:167], v[64:67], v[8:11]
	v_add_f32_e32 v194, v194, v81
	v_add_f32_e32 v194, v194, v82
	v_add_f32_e32 v194, v194, v83
	ds_read_b128 v[164:167], v224 offset:2048
	v_mfma_f32_16x16x32_bf16 v[16:19], v[168:171], v[64:67], v[16:19]
	v_add_f32_e32 v195, v195, v84
	v_add_f32_e32 v195, v195, v85
	v_add_f32_e32 v195, v195, v86
	v_mfma_f32_16x16x32_bf16 v[20:23], v[168:171], v[68:71], v[20:23]
	v_add_f32_e32 v195, v195, v87
	v_cvt_pk_bf16_f32 v80, v80, v81
	v_cvt_pk_bf16_f32 v81, v82, v83
	ds_read_b128 v[168:171], v224 offset:4096
	v_mfma_f32_16x16x32_bf16 v[28:31], v[172:175], v[68:71], v[28:31]
	v_cvt_pk_bf16_f32 v84, v84, v85
	v_cvt_pk_bf16_f32 v85, v86, v87
	v_mfma_f32_16x16x32_bf16 v[24:27], v[172:175], v[64:67], v[24:27]
	ds_read_b128 v[172:175], v224 offset:6144
	s_waitcnt lgkmcnt(4)
	v_mfma_f32_16x16x32_bf16 v[32:35], v[176:179], v[64:67], v[32:35]
	v_exp_f32_e32 v88, v88
	v_exp_f32_e32 v89, v89
	v_exp_f32_e32 v90, v90
	v_mfma_f32_16x16x32_bf16 v[36:39], v[176:179], v[68:71], v[36:39]
	v_exp_f32_e32 v91, v91
	v_exp_f32_e32 v92, v92
	v_exp_f32_e32 v93, v93
	ds_read_b128 v[176:179], v224 offset:8192
	v_mfma_f32_16x16x32_bf16 v[44:47], v[180:183], v[68:71], v[44:47]
	v_exp_f32_e32 v94, v94
	v_exp_f32_e32 v95, v95
	v_add_f32_e32 v194, v194, v88
	v_mfma_f32_16x16x32_bf16 v[40:43], v[180:183], v[64:67], v[40:43]
	v_add_f32_e32 v194, v194, v89
	v_add_f32_e32 v194, v194, v90
	v_add_f32_e32 v194, v194, v91
	ds_read_b128 v[180:183], v224 offset:10240
	v_mfma_f32_16x16x32_bf16 v[48:51], v[230:233], v[64:67], v[48:51]
	v_add_f32_e32 v195, v195, v92
	v_add_f32_e32 v195, v195, v93
	v_add_f32_e32 v195, v195, v94
	v_mfma_f32_16x16x32_bf16 v[52:55], v[230:233], v[68:71], v[52:55]
	v_add_f32_e32 v195, v195, v95
	v_cvt_pk_bf16_f32 v82, v88, v89
	v_cvt_pk_bf16_f32 v83, v90, v91
	ds_read_b128 v[230:233], v224 offset:12288
	v_mfma_f32_16x16x32_bf16 v[60:63], v[234:237], v[68:71], v[60:63]
	v_cvt_pk_bf16_f32 v86, v92, v93
	v_cvt_pk_bf16_f32 v87, v94, v95
	v_mfma_f32_16x16x32_bf16 v[56:59], v[234:237], v[64:67], v[56:59]
	ds_read_b128 v[234:237], v224 offset:14336
	s_waitcnt lgkmcnt(7)
	v_mfma_f32_16x16x32_bf16 v[0:3], v[160:163], v[80:83], v[0:3]
	v_mfma_f32_16x16x32_bf16 v[4:7], v[160:163], v[84:87], v[4:7]
	ds_read_b128 v[160:163], v201 offset:0
	s_waitcnt lgkmcnt(7)
	v_mfma_f32_16x16x32_bf16 v[12:15], v[164:167], v[84:87], v[12:15]
	v_mfma_f32_16x16x32_bf16 v[8:11], v[164:167], v[80:83], v[8:11]
	ds_read_b128 v[164:167], v202 offset:0
	s_waitcnt lgkmcnt(7)
	v_mfma_f32_16x16x32_bf16 v[16:19], v[168:171], v[80:83], v[16:19]
	v_mfma_f32_16x16x32_bf16 v[20:23], v[168:171], v[84:87], v[20:23]
	ds_read_b128 v[168:171], v203 offset:0
	s_waitcnt lgkmcnt(7)
	v_mfma_f32_16x16x32_bf16 v[28:31], v[172:175], v[84:87], v[28:31]
	v_mfma_f32_16x16x32_bf16 v[24:27], v[172:175], v[80:83], v[24:27]
	ds_read_b128 v[172:175], v204 offset:0
	s_waitcnt lgkmcnt(7)
	v_mfma_f32_16x16x32_bf16 v[32:35], v[176:179], v[80:83], v[32:35]
	v_mfma_f32_16x16x32_bf16 v[36:39], v[176:179], v[84:87], v[36:39]
	ds_read_b128 v[176:179], v201 offset:4096
	s_waitcnt lgkmcnt(7)
	v_mfma_f32_16x16x32_bf16 v[44:47], v[180:183], v[84:87], v[44:47]
	v_mfma_f32_16x16x32_bf16 v[40:43], v[180:183], v[80:83], v[40:43]
	ds_read_b128 v[180:183], v202 offset:4096
	s_waitcnt lgkmcnt(7)
	v_mfma_f32_16x16x32_bf16 v[48:51], v[230:233], v[80:83], v[48:51]
	v_mfma_f32_16x16x32_bf16 v[52:55], v[230:233], v[84:87], v[52:55]
	ds_read_b128 v[230:233], v203 offset:4096
	s_waitcnt lgkmcnt(7)
	v_mfma_f32_16x16x32_bf16 v[60:63], v[234:237], v[84:87], v[60:63]
	v_mfma_f32_16x16x32_bf16 v[56:59], v[234:237], v[80:83], v[56:59]
	ds_read_b128 v[234:237], v204 offset:4096
	s_waitcnt lgkmcnt(7)
	v_mfma_f32_16x16x32_bf16 v[64:67], v[160:163], v[96:99], 0
	s_waitcnt lgkmcnt(6)
	v_mfma_f32_16x16x32_bf16 v[64:67], v[164:167], v[100:103], v[64:67]
	s_add_u32 s100, s100, 0x4000
	s_cmp_eq_u32 s100, 0x10000
	s_cselect_b32 s100, 0x24000, s100
	s_cmp_eq_u32 s100, 0x28000
	s_cselect_b32 s100, 0, s100
	s_add_u32 s101, s101, 0x4000
	s_cmp_eq_u32 s101, 0x10000
	s_cselect_b32 s101, 0x24000, s101
	s_cmp_eq_u32 s101, 0x28000
	s_cselect_b32 s101, 0, s101
	v_add_u32_e32 v211, s100, v209
	v_add_u32_e32 v224, s100, v210
	v_add_u32_e32 v229, s101, v227
	v_add_u32_e32 v184, s101, v228
	s_add_u32 s16, s22, s10
	s_addc_u32 s17, s23, s11
	s_add_u32 s15, s22, s12
	s_addc_u32 s14, s23, s13
	s_add_u32 s8, s16, 0x3bc00200
	s_addc_u32 s9, s17, 0
	s_add_u32 s6, s15, 0x23a40000
	s_addc_u32 s7, s14, 0
	s_waitcnt lgkmcnt(5)
	v_mfma_f32_16x16x32_bf16 v[64:67], v[168:171], v[104:107], v[64:67]
	s_waitcnt lgkmcnt(4)
	v_mfma_f32_16x16x32_bf16 v[64:67], v[172:175], v[108:111], v[64:67]
	s_waitcnt vmcnt(4)
	ds_write_b128 v225, v[136:139] offset:32768
	v_mfma_f32_16x16x32_bf16 v[68:71], v[172:175], v[124:127], 0
	ds_read_b128 v[172:175], v204 offset:8192
	v_mfma_f32_16x16x32_bf16 v[68:71], v[168:171], v[120:123], v[68:71]
	ds_read_b128 v[168:171], v203 offset:8192
	ds_write_b128 v226, v[140:143] offset:32768
	v_mfma_f32_16x16x32_bf16 v[68:71], v[164:167], v[116:119], v[68:71]
	ds_read_b128 v[164:167], v202 offset:8192
	v_mfma_f32_16x16x32_bf16 v[68:71], v[160:163], v[112:115], v[68:71]
	ds_read_b128 v[160:163], v201 offset:8192
	ds_write_b64 v229, v[132:133] offset:0
	s_waitcnt lgkmcnt(10)
	v_mfma_f32_16x16x32_bf16 v[72:75], v[176:179], v[96:99], 0
	s_waitcnt lgkmcnt(9)
	v_mfma_f32_16x16x32_bf16 v[72:75], v[180:183], v[100:103], v[72:75]
	ds_write_b64 v184, v[134:135] offset:0
	s_waitcnt lgkmcnt(9)
	v_mfma_f32_16x16x32_bf16 v[72:75], v[230:233], v[104:107], v[72:75]
	s_waitcnt lgkmcnt(8)
	v_mfma_f32_16x16x32_bf16 v[72:75], v[234:237], v[108:111], v[72:75]
	ds_write_b64 v229, v[128:129] offset:8192
	v_mfma_f32_16x16x32_bf16 v[76:79], v[234:237], v[124:127], 0
	ds_read_b128 v[234:237], v204 offset:12288
	v_mfma_f32_16x16x32_bf16 v[76:79], v[230:233], v[120:123], v[76:79]
	ds_read_b128 v[230:233], v203 offset:12288
	ds_write_b64 v184, v[130:131] offset:8192
	v_mfma_f32_16x16x32_bf16 v[76:79], v[180:183], v[116:119], v[76:79]
	ds_read_b128 v[180:183], v202 offset:12288
	v_mfma_f32_16x16x32_bf16 v[76:79], v[176:179], v[112:115], v[76:79]
	ds_read_b128 v[176:179], v201 offset:12288
	global_load_dwordx4 v[132:135], v198, s[8:9]
	s_waitcnt lgkmcnt(8)
	v_mfma_f32_16x16x32_bf16 v[80:83], v[160:163], v[96:99], 0
	v_exp_f32_e32 v64, v64
	v_exp_f32_e32 v65, v65
	v_exp_f32_e32 v66, v66
	v_mfma_f32_16x16x32_bf16 v[80:83], v[164:167], v[100:103], v[80:83]
	v_exp_f32_e32 v67, v67
	v_exp_f32_e32 v68, v68
	v_exp_f32_e32 v69, v69
	global_load_dwordx4 v[128:131], v199, s[8:9]
	v_mfma_f32_16x16x32_bf16 v[80:83], v[168:171], v[104:107], v[80:83]
	v_exp_f32_e32 v70, v70
	v_exp_f32_e32 v71, v71
	v_add_f32_e32 v194, v194, v64
	v_mfma_f32_16x16x32_bf16 v[80:83], v[172:175], v[108:111], v[80:83]
	v_add_f32_e32 v194, v194, v65
	v_add_f32_e32 v194, v194, v66
	v_add_f32_e32 v194, v194, v67
	global_load_dwordx4 v[136:139], v196, s[6:7]
	v_mfma_f32_16x16x32_bf16 v[84:87], v[172:175], v[124:127], 0
	v_add_f32_e32 v195, v195, v68
	v_add_f32_e32 v195, v195, v69
	v_add_f32_e32 v195, v195, v70
	ds_read_b128 v[172:175], v211 offset:6144
	v_mfma_f32_16x16x32_bf16 v[84:87], v[168:171], v[120:123], v[84:87]
	v_add_f32_e32 v195, v195, v71
	v_cvt_pk_bf16_f32 v64, v64, v65
	v_cvt_pk_bf16_f32 v65, v66, v67
	ds_read_b128 v[168:171], v211 offset:4096
	global_load_dwordx4 v[140:143], v197, s[6:7]
	v_mfma_f32_16x16x32_bf16 v[84:87], v[164:167], v[116:119], v[84:87]
	v_cvt_pk_bf16_f32 v68, v68, v69
	v_cvt_pk_bf16_f32 v69, v70, v71
	ds_read_b128 v[164:167], v211 offset:2048
	v_mfma_f32_16x16x32_bf16 v[84:87], v[160:163], v[112:115], v[84:87]
	ds_read_b128 v[160:163], v211 offset:0
	s_waitcnt lgkmcnt(4)
	v_mfma_f32_16x16x32_bf16 v[88:91], v[176:179], v[96:99], 0
	v_exp_f32_e32 v72, v72
	v_exp_f32_e32 v73, v73
	v_exp_f32_e32 v74, v74
	v_mfma_f32_16x16x32_bf16 v[88:91], v[180:183], v[100:103], v[88:91]
	v_exp_f32_e32 v75, v75
	v_exp_f32_e32 v76, v76
	v_exp_f32_e32 v77, v77
	v_mfma_f32_16x16x32_bf16 v[88:91], v[230:233], v[104:107], v[88:91]
	v_exp_f32_e32 v78, v78
	v_exp_f32_e32 v79, v79
	v_add_f32_e32 v194, v194, v72
	v_mfma_f32_16x16x32_bf16 v[88:91], v[234:237], v[108:111], v[88:91]
	v_add_f32_e32 v194, v194, v73
	v_add_f32_e32 v194, v194, v74
	v_add_f32_e32 v194, v194, v75
	v_mfma_f32_16x16x32_bf16 v[92:95], v[234:237], v[124:127], 0
	v_add_f32_e32 v195, v195, v76
	v_add_f32_e32 v195, v195, v77
	v_add_f32_e32 v195, v195, v78
	ds_read_b128 v[234:237], v211 offset:14336
	v_mfma_f32_16x16x32_bf16 v[92:95], v[230:233], v[120:123], v[92:95]
	v_add_f32_e32 v195, v195, v79
	v_cvt_pk_bf16_f32 v66, v72, v73
	v_cvt_pk_bf16_f32 v67, v74, v75
	ds_read_b128 v[230:233], v211 offset:12288
	v_mfma_f32_16x16x32_bf16 v[92:95], v[180:183], v[116:119], v[92:95]
	v_cvt_pk_bf16_f32 v70, v76, v77
	v_cvt_pk_bf16_f32 v71, v78, v79
	ds_read_b128 v[180:183], v211 offset:10240
	v_mfma_f32_16x16x32_bf16 v[92:95], v[176:179], v[112:115], v[92:95]
	ds_read_b128 v[176:179], v211 offset:8192
	s_waitcnt lgkmcnt(4)
	v_mfma_f32_16x16x32_bf16 v[0:3], v[160:163], v[64:67], v[0:3]
	v_exp_f32_e32 v80, v80
	v_exp_f32_e32 v81, v81
	v_exp_f32_e32 v82, v82
	v_mfma_f32_16x16x32_bf16 v[4:7], v[160:163], v[68:71], v[4:7]
	v_exp_f32_e32 v83, v83
	v_exp_f32_e32 v84, v84
	v_exp_f32_e32 v85, v85
	ds_read_b128 v[160:163], v224 offset:0
	v_mfma_f32_16x16x32_bf16 v[12:15], v[164:167], v[68:71], v[12:15]
	v_exp_f32_e32 v86, v86
	v_exp_f32_e32 v87, v87
	v_add_f32_e32 v194, v194, v80
	v_mfma_f32_16x16x32_bf16 v[8:11], v[164:167], v[64:67], v[8:11]
	v_add_f32_e32 v194, v194, v81
	v_add_f32_e32 v194, v194, v82
	v_add_f32_e32 v194, v194, v83
	ds_read_b128 v[164:167], v224 offset:2048
	v_mfma_f32_16x16x32_bf16 v[16:19], v[168:171], v[64:67], v[16:19]
	v_add_f32_e32 v195, v195, v84
	v_add_f32_e32 v195, v195, v85
	v_add_f32_e32 v195, v195, v86
	v_mfma_f32_16x16x32_bf16 v[20:23], v[168:171], v[68:71], v[20:23]
	v_add_f32_e32 v195, v195, v87
	v_cvt_pk_bf16_f32 v80, v80, v81
	v_cvt_pk_bf16_f32 v81, v82, v83
	ds_read_b128 v[168:171], v224 offset:4096
	v_mfma_f32_16x16x32_bf16 v[28:31], v[172:175], v[68:71], v[28:31]
	v_cvt_pk_bf16_f32 v84, v84, v85
	v_cvt_pk_bf16_f32 v85, v86, v87
	v_mfma_f32_16x16x32_bf16 v[24:27], v[172:175], v[64:67], v[24:27]
	ds_read_b128 v[172:175], v224 offset:6144
	s_waitcnt lgkmcnt(4)
	v_mfma_f32_16x16x32_bf16 v[32:35], v[176:179], v[64:67], v[32:35]
	v_exp_f32_e32 v88, v88
	v_exp_f32_e32 v89, v89
	v_exp_f32_e32 v90, v90
	v_mfma_f32_16x16x32_bf16 v[36:39], v[176:179], v[68:71], v[36:39]
	v_exp_f32_e32 v91, v91
	v_exp_f32_e32 v92, v92
	v_exp_f32_e32 v93, v93
	ds_read_b128 v[176:179], v224 offset:8192
	v_mfma_f32_16x16x32_bf16 v[44:47], v[180:183], v[68:71], v[44:47]
	v_exp_f32_e32 v94, v94
	v_exp_f32_e32 v95, v95
	v_add_f32_e32 v194, v194, v88
	v_mfma_f32_16x16x32_bf16 v[40:43], v[180:183], v[64:67], v[40:43]
	v_add_f32_e32 v194, v194, v89
	v_add_f32_e32 v194, v194, v90
	v_add_f32_e32 v194, v194, v91
	ds_read_b128 v[180:183], v224 offset:10240
	v_mfma_f32_16x16x32_bf16 v[48:51], v[230:233], v[64:67], v[48:51]
	v_add_f32_e32 v195, v195, v92
	v_add_f32_e32 v195, v195, v93
	v_add_f32_e32 v195, v195, v94
	v_mfma_f32_16x16x32_bf16 v[52:55], v[230:233], v[68:71], v[52:55]
	v_add_f32_e32 v195, v195, v95
	v_cvt_pk_bf16_f32 v82, v88, v89
	v_cvt_pk_bf16_f32 v83, v90, v91
	ds_read_b128 v[230:233], v224 offset:12288
	v_mfma_f32_16x16x32_bf16 v[60:63], v[234:237], v[68:71], v[60:63]
	v_cvt_pk_bf16_f32 v86, v92, v93
	v_cvt_pk_bf16_f32 v87, v94, v95
	v_mfma_f32_16x16x32_bf16 v[56:59], v[234:237], v[64:67], v[56:59]
	ds_read_b128 v[234:237], v224 offset:14336
	s_waitcnt lgkmcnt(7)
	v_mfma_f32_16x16x32_bf16 v[0:3], v[160:163], v[80:83], v[0:3]
	v_mfma_f32_16x16x32_bf16 v[4:7], v[160:163], v[84:87], v[4:7]
	ds_read_b128 v[160:163], v201 offset:16384
	s_waitcnt lgkmcnt(7)
	v_mfma_f32_16x16x32_bf16 v[12:15], v[164:167], v[84:87], v[12:15]
	v_mfma_f32_16x16x32_bf16 v[8:11], v[164:167], v[80:83], v[8:11]
	ds_read_b128 v[164:167], v202 offset:16384
	s_waitcnt lgkmcnt(7)
	v_mfma_f32_16x16x32_bf16 v[16:19], v[168:171], v[80:83], v[16:19]
	v_mfma_f32_16x16x32_bf16 v[20:23], v[168:171], v[84:87], v[20:23]
	ds_read_b128 v[168:171], v203 offset:16384
	s_waitcnt lgkmcnt(7)
	v_mfma_f32_16x16x32_bf16 v[28:31], v[172:175], v[84:87], v[28:31]
	v_mfma_f32_16x16x32_bf16 v[24:27], v[172:175], v[80:83], v[24:27]
	ds_read_b128 v[172:175], v204 offset:16384
	s_waitcnt lgkmcnt(7)
	v_mfma_f32_16x16x32_bf16 v[32:35], v[176:179], v[80:83], v[32:35]
	v_mfma_f32_16x16x32_bf16 v[36:39], v[176:179], v[84:87], v[36:39]
	ds_read_b128 v[176:179], v201 offset:20480
	s_waitcnt lgkmcnt(7)
	v_mfma_f32_16x16x32_bf16 v[44:47], v[180:183], v[84:87], v[44:47]
	v_mfma_f32_16x16x32_bf16 v[40:43], v[180:183], v[80:83], v[40:43]
	ds_read_b128 v[180:183], v202 offset:20480
	s_waitcnt lgkmcnt(7)
	v_mfma_f32_16x16x32_bf16 v[48:51], v[230:233], v[80:83], v[48:51]
	v_mfma_f32_16x16x32_bf16 v[52:55], v[230:233], v[84:87], v[52:55]
	ds_read_b128 v[230:233], v203 offset:20480
	s_waitcnt lgkmcnt(7)
	v_mfma_f32_16x16x32_bf16 v[60:63], v[234:237], v[84:87], v[60:63]
	v_mfma_f32_16x16x32_bf16 v[56:59], v[234:237], v[80:83], v[56:59]
	ds_read_b128 v[234:237], v204 offset:20480
	s_waitcnt lgkmcnt(7)
	v_mfma_f32_16x16x32_bf16 v[64:67], v[160:163], v[96:99], 0
	s_waitcnt lgkmcnt(6)
	v_mfma_f32_16x16x32_bf16 v[64:67], v[164:167], v[100:103], v[64:67]
	s_add_u32 s100, s100, 0x4000
	s_cmp_eq_u32 s100, 0x10000
	s_cselect_b32 s100, 0x24000, s100
	s_cmp_eq_u32 s100, 0x28000
	s_cselect_b32 s100, 0, s100
	s_add_u32 s101, s101, 0x4000
	s_cmp_eq_u32 s101, 0x10000
	s_cselect_b32 s101, 0x24000, s101
	s_cmp_eq_u32 s101, 0x28000
	s_cselect_b32 s101, 0, s101
	v_add_u32_e32 v211, s100, v209
	v_add_u32_e32 v224, s100, v210
	v_add_u32_e32 v229, s101, v227
	v_add_u32_e32 v184, s101, v228
	s_add_u32 s8, s16, 0x3bc00280
	s_addc_u32 s9, s17, 0
	s_add_u32 s6, s15, 0x23a50000
	s_addc_u32 s7, s14, 0
	s_waitcnt lgkmcnt(5)
	v_mfma_f32_16x16x32_bf16 v[64:67], v[168:171], v[104:107], v[64:67]
	s_waitcnt lgkmcnt(4)
	v_mfma_f32_16x16x32_bf16 v[64:67], v[172:175], v[108:111], v[64:67]
	s_waitcnt vmcnt(4)
	ds_write_b128 v225, v[152:155] offset:49152
	v_mfma_f32_16x16x32_bf16 v[68:71], v[172:175], v[124:127], 0
	ds_read_b128 v[172:175], v204 offset:24576
	v_mfma_f32_16x16x32_bf16 v[68:71], v[168:171], v[120:123], v[68:71]
	ds_read_b128 v[168:171], v203 offset:24576
	ds_write_b128 v226, v[156:159] offset:49152
	v_mfma_f32_16x16x32_bf16 v[68:71], v[164:167], v[116:119], v[68:71]
	ds_read_b128 v[164:167], v202 offset:24576
	v_mfma_f32_16x16x32_bf16 v[68:71], v[160:163], v[112:115], v[68:71]
	ds_read_b128 v[160:163], v201 offset:24576
	ds_write_b64 v229, v[148:149] offset:0
	s_waitcnt lgkmcnt(10)
	v_mfma_f32_16x16x32_bf16 v[72:75], v[176:179], v[96:99], 0
	s_waitcnt lgkmcnt(9)
	v_mfma_f32_16x16x32_bf16 v[72:75], v[180:183], v[100:103], v[72:75]
	ds_write_b64 v184, v[150:151] offset:0
	s_waitcnt lgkmcnt(9)
	v_mfma_f32_16x16x32_bf16 v[72:75], v[230:233], v[104:107], v[72:75]
	s_waitcnt lgkmcnt(8)
	v_mfma_f32_16x16x32_bf16 v[72:75], v[234:237], v[108:111], v[72:75]
	ds_write_b64 v229, v[144:145] offset:8192
	v_mfma_f32_16x16x32_bf16 v[76:79], v[234:237], v[124:127], 0
	ds_read_b128 v[234:237], v204 offset:28672
	v_mfma_f32_16x16x32_bf16 v[76:79], v[230:233], v[120:123], v[76:79]
	ds_read_b128 v[230:233], v203 offset:28672
	ds_write_b64 v184, v[146:147] offset:8192
	v_mfma_f32_16x16x32_bf16 v[76:79], v[180:183], v[116:119], v[76:79]
	ds_read_b128 v[180:183], v202 offset:28672
	v_mfma_f32_16x16x32_bf16 v[76:79], v[176:179], v[112:115], v[76:79]
	ds_read_b128 v[176:179], v201 offset:28672
	global_load_dwordx4 v[148:151], v198, s[8:9]
	s_waitcnt lgkmcnt(8)
	v_mfma_f32_16x16x32_bf16 v[80:83], v[160:163], v[96:99], 0
	v_exp_f32_e32 v64, v64
	v_exp_f32_e32 v65, v65
	v_exp_f32_e32 v66, v66
	v_mfma_f32_16x16x32_bf16 v[80:83], v[164:167], v[100:103], v[80:83]
	v_exp_f32_e32 v67, v67
	v_exp_f32_e32 v68, v68
	v_exp_f32_e32 v69, v69
	global_load_dwordx4 v[144:147], v199, s[8:9]
	v_mfma_f32_16x16x32_bf16 v[80:83], v[168:171], v[104:107], v[80:83]
	v_exp_f32_e32 v70, v70
	v_exp_f32_e32 v71, v71
	v_add_f32_e32 v194, v194, v64
	v_mfma_f32_16x16x32_bf16 v[80:83], v[172:175], v[108:111], v[80:83]
	v_add_f32_e32 v194, v194, v65
	v_add_f32_e32 v194, v194, v66
	v_add_f32_e32 v194, v194, v67
	global_load_dwordx4 v[152:155], v196, s[6:7]
	v_mfma_f32_16x16x32_bf16 v[84:87], v[172:175], v[124:127], 0
	v_add_f32_e32 v195, v195, v68
	v_add_f32_e32 v195, v195, v69
	v_add_f32_e32 v195, v195, v70
	ds_read_b128 v[172:175], v211 offset:6144
	v_mfma_f32_16x16x32_bf16 v[84:87], v[168:171], v[120:123], v[84:87]
	v_add_f32_e32 v195, v195, v71
	v_cvt_pk_bf16_f32 v64, v64, v65
	v_cvt_pk_bf16_f32 v65, v66, v67
	ds_read_b128 v[168:171], v211 offset:4096
	global_load_dwordx4 v[156:159], v197, s[6:7]
	v_mfma_f32_16x16x32_bf16 v[84:87], v[164:167], v[116:119], v[84:87]
	v_cvt_pk_bf16_f32 v68, v68, v69
	v_cvt_pk_bf16_f32 v69, v70, v71
	ds_read_b128 v[164:167], v211 offset:2048
	v_mfma_f32_16x16x32_bf16 v[84:87], v[160:163], v[112:115], v[84:87]
	ds_read_b128 v[160:163], v211 offset:0
	s_waitcnt lgkmcnt(4)
	v_mfma_f32_16x16x32_bf16 v[88:91], v[176:179], v[96:99], 0
	v_exp_f32_e32 v72, v72
	v_exp_f32_e32 v73, v73
	v_exp_f32_e32 v74, v74
	v_mfma_f32_16x16x32_bf16 v[88:91], v[180:183], v[100:103], v[88:91]
	v_exp_f32_e32 v75, v75
	v_exp_f32_e32 v76, v76
	v_exp_f32_e32 v77, v77
	v_mfma_f32_16x16x32_bf16 v[88:91], v[230:233], v[104:107], v[88:91]
	v_exp_f32_e32 v78, v78
	v_exp_f32_e32 v79, v79
	v_add_f32_e32 v194, v194, v72
	v_mfma_f32_16x16x32_bf16 v[88:91], v[234:237], v[108:111], v[88:91]
	v_add_f32_e32 v194, v194, v73
	v_add_f32_e32 v194, v194, v74
	v_add_f32_e32 v194, v194, v75
	v_mfma_f32_16x16x32_bf16 v[92:95], v[234:237], v[124:127], 0
	v_add_f32_e32 v195, v195, v76
	v_add_f32_e32 v195, v195, v77
	v_add_f32_e32 v195, v195, v78
	ds_read_b128 v[234:237], v211 offset:14336
	v_mfma_f32_16x16x32_bf16 v[92:95], v[230:233], v[120:123], v[92:95]
	v_add_f32_e32 v195, v195, v79
	v_cvt_pk_bf16_f32 v66, v72, v73
	v_cvt_pk_bf16_f32 v67, v74, v75
	ds_read_b128 v[230:233], v211 offset:12288
	v_mfma_f32_16x16x32_bf16 v[92:95], v[180:183], v[116:119], v[92:95]
	v_cvt_pk_bf16_f32 v70, v76, v77
	v_cvt_pk_bf16_f32 v71, v78, v79
	ds_read_b128 v[180:183], v211 offset:10240
	v_mfma_f32_16x16x32_bf16 v[92:95], v[176:179], v[112:115], v[92:95]
	ds_read_b128 v[176:179], v211 offset:8192
	s_barrier
	s_waitcnt lgkmcnt(4)
	v_mfma_f32_16x16x32_bf16 v[0:3], v[160:163], v[64:67], v[0:3]
	v_exp_f32_e32 v80, v80
	v_exp_f32_e32 v81, v81
	v_exp_f32_e32 v82, v82
	v_mfma_f32_16x16x32_bf16 v[4:7], v[160:163], v[68:71], v[4:7]
	v_exp_f32_e32 v83, v83
	v_exp_f32_e32 v84, v84
	v_exp_f32_e32 v85, v85
	ds_read_b128 v[160:163], v224 offset:0
	v_mfma_f32_16x16x32_bf16 v[12:15], v[164:167], v[68:71], v[12:15]
	v_exp_f32_e32 v86, v86
	v_exp_f32_e32 v87, v87
	v_add_f32_e32 v194, v194, v80
	v_mfma_f32_16x16x32_bf16 v[8:11], v[164:167], v[64:67], v[8:11]
	v_add_f32_e32 v194, v194, v81
	v_add_f32_e32 v194, v194, v82
	v_add_f32_e32 v194, v194, v83
	ds_read_b128 v[164:167], v224 offset:2048
	v_mfma_f32_16x16x32_bf16 v[16:19], v[168:171], v[64:67], v[16:19]
	v_add_f32_e32 v195, v195, v84
	v_add_f32_e32 v195, v195, v85
	v_add_f32_e32 v195, v195, v86
	v_mfma_f32_16x16x32_bf16 v[20:23], v[168:171], v[68:71], v[20:23]
	v_add_f32_e32 v195, v195, v87
	v_cvt_pk_bf16_f32 v80, v80, v81
	v_cvt_pk_bf16_f32 v81, v82, v83
	ds_read_b128 v[168:171], v224 offset:4096
	v_mfma_f32_16x16x32_bf16 v[28:31], v[172:175], v[68:71], v[28:31]
	v_cvt_pk_bf16_f32 v84, v84, v85
	v_cvt_pk_bf16_f32 v85, v86, v87
	v_mfma_f32_16x16x32_bf16 v[24:27], v[172:175], v[64:67], v[24:27]
	ds_read_b128 v[172:175], v224 offset:6144
	s_waitcnt lgkmcnt(4)
	v_mfma_f32_16x16x32_bf16 v[32:35], v[176:179], v[64:67], v[32:35]
	v_exp_f32_e32 v88, v88
	v_exp_f32_e32 v89, v89
	v_exp_f32_e32 v90, v90
	v_mfma_f32_16x16x32_bf16 v[36:39], v[176:179], v[68:71], v[36:39]
	v_exp_f32_e32 v91, v91
	v_exp_f32_e32 v92, v92
	v_exp_f32_e32 v93, v93
	ds_read_b128 v[176:179], v224 offset:8192
	v_mfma_f32_16x16x32_bf16 v[44:47], v[180:183], v[68:71], v[44:47]
	v_exp_f32_e32 v94, v94
	v_exp_f32_e32 v95, v95
	v_add_f32_e32 v194, v194, v88
	v_mfma_f32_16x16x32_bf16 v[40:43], v[180:183], v[64:67], v[40:43]
	v_add_f32_e32 v194, v194, v89
	v_add_f32_e32 v194, v194, v90
	v_add_f32_e32 v194, v194, v91
	ds_read_b128 v[180:183], v224 offset:10240
	v_mfma_f32_16x16x32_bf16 v[48:51], v[230:233], v[64:67], v[48:51]
	v_add_f32_e32 v195, v195, v92
	v_add_f32_e32 v195, v195, v93
	v_add_f32_e32 v195, v195, v94
	v_mfma_f32_16x16x32_bf16 v[52:55], v[230:233], v[68:71], v[52:55]
	v_add_f32_e32 v195, v195, v95
	v_cvt_pk_bf16_f32 v82, v88, v89
	v_cvt_pk_bf16_f32 v83, v90, v91
	ds_read_b128 v[230:233], v224 offset:12288
	v_mfma_f32_16x16x32_bf16 v[60:63], v[234:237], v[68:71], v[60:63]
	v_cvt_pk_bf16_f32 v86, v92, v93
	v_cvt_pk_bf16_f32 v87, v94, v95
	v_mfma_f32_16x16x32_bf16 v[56:59], v[234:237], v[64:67], v[56:59]
	ds_read_b128 v[234:237], v224 offset:14336
	s_waitcnt lgkmcnt(7)
	v_mfma_f32_16x16x32_bf16 v[0:3], v[160:163], v[80:83], v[0:3]
	v_mfma_f32_16x16x32_bf16 v[4:7], v[160:163], v[84:87], v[4:7]
	ds_read_b128 v[160:163], v201 offset:32768
	s_waitcnt lgkmcnt(7)
	v_mfma_f32_16x16x32_bf16 v[12:15], v[164:167], v[84:87], v[12:15]
	v_mfma_f32_16x16x32_bf16 v[8:11], v[164:167], v[80:83], v[8:11]
	ds_read_b128 v[164:167], v202 offset:32768
	s_waitcnt lgkmcnt(7)
	v_mfma_f32_16x16x32_bf16 v[16:19], v[168:171], v[80:83], v[16:19]
	v_mfma_f32_16x16x32_bf16 v[20:23], v[168:171], v[84:87], v[20:23]
	ds_read_b128 v[168:171], v203 offset:32768
	s_waitcnt lgkmcnt(7)
	v_mfma_f32_16x16x32_bf16 v[28:31], v[172:175], v[84:87], v[28:31]
	v_mfma_f32_16x16x32_bf16 v[24:27], v[172:175], v[80:83], v[24:27]
	ds_read_b128 v[172:175], v204 offset:32768
	s_waitcnt lgkmcnt(7)
	v_mfma_f32_16x16x32_bf16 v[32:35], v[176:179], v[80:83], v[32:35]
	v_mfma_f32_16x16x32_bf16 v[36:39], v[176:179], v[84:87], v[36:39]
	ds_read_b128 v[176:179], v201 offset:36864
	s_waitcnt lgkmcnt(7)
	v_mfma_f32_16x16x32_bf16 v[44:47], v[180:183], v[84:87], v[44:47]
	v_mfma_f32_16x16x32_bf16 v[40:43], v[180:183], v[80:83], v[40:43]
	ds_read_b128 v[180:183], v202 offset:36864
	s_waitcnt lgkmcnt(7)
	v_mfma_f32_16x16x32_bf16 v[48:51], v[230:233], v[80:83], v[48:51]
	v_mfma_f32_16x16x32_bf16 v[52:55], v[230:233], v[84:87], v[52:55]
	ds_read_b128 v[230:233], v203 offset:36864
	s_waitcnt lgkmcnt(7)
	v_mfma_f32_16x16x32_bf16 v[60:63], v[234:237], v[84:87], v[60:63]
	v_mfma_f32_16x16x32_bf16 v[56:59], v[234:237], v[80:83], v[56:59]
	ds_read_b128 v[234:237], v204 offset:36864
	s_waitcnt lgkmcnt(7)
	v_mfma_f32_16x16x32_bf16 v[64:67], v[160:163], v[96:99], 0
	s_waitcnt lgkmcnt(6)
	v_mfma_f32_16x16x32_bf16 v[64:67], v[164:167], v[100:103], v[64:67]
	s_add_u32 s100, s100, 0x4000
	s_cmp_eq_u32 s100, 0x10000
	s_cselect_b32 s100, 0x24000, s100
	s_cmp_eq_u32 s100, 0x28000
	s_cselect_b32 s100, 0, s100
	s_add_u32 s101, s101, 0x4000
	s_cmp_eq_u32 s101, 0x10000
	s_cselect_b32 s101, 0x24000, s101
	s_cmp_eq_u32 s101, 0x28000
	s_cselect_b32 s101, 0, s101
	v_add_u32_e32 v211, s100, v209
	v_add_u32_e32 v224, s100, v210
	v_add_u32_e32 v229, s101, v227
	v_add_u32_e32 v184, s101, v228
	s_add_u32 s8, s16, 0x3bc00300
	s_addc_u32 s9, s17, 0
	s_add_u32 s6, s15, 0x23a60000
	s_addc_u32 s7, s14, 0
	s_waitcnt lgkmcnt(5)
	v_mfma_f32_16x16x32_bf16 v[64:67], v[168:171], v[104:107], v[64:67]
	s_waitcnt lgkmcnt(4)
	v_mfma_f32_16x16x32_bf16 v[64:67], v[172:175], v[108:111], v[64:67]
	s_waitcnt vmcnt(4)
	ds_write_b128 v225, v[136:139] offset:0
	v_mfma_f32_16x16x32_bf16 v[68:71], v[172:175], v[124:127], 0
	ds_read_b128 v[172:175], v204 offset:40960
	v_mfma_f32_16x16x32_bf16 v[68:71], v[168:171], v[120:123], v[68:71]
	ds_read_b128 v[168:171], v203 offset:40960
	ds_write_b128 v226, v[140:143] offset:0
	v_mfma_f32_16x16x32_bf16 v[68:71], v[164:167], v[116:119], v[68:71]
	ds_read_b128 v[164:167], v202 offset:40960
	v_mfma_f32_16x16x32_bf16 v[68:71], v[160:163], v[112:115], v[68:71]
	ds_read_b128 v[160:163], v201 offset:40960
	ds_write_b64 v229, v[132:133] offset:0
	s_waitcnt lgkmcnt(10)
	v_mfma_f32_16x16x32_bf16 v[72:75], v[176:179], v[96:99], 0
	s_waitcnt lgkmcnt(9)
	v_mfma_f32_16x16x32_bf16 v[72:75], v[180:183], v[100:103], v[72:75]
	ds_write_b64 v184, v[134:135] offset:0
	s_waitcnt lgkmcnt(9)
	v_mfma_f32_16x16x32_bf16 v[72:75], v[230:233], v[104:107], v[72:75]
	s_waitcnt lgkmcnt(8)
	v_mfma_f32_16x16x32_bf16 v[72:75], v[234:237], v[108:111], v[72:75]
	ds_write_b64 v229, v[128:129] offset:8192
	v_mfma_f32_16x16x32_bf16 v[76:79], v[234:237], v[124:127], 0
	ds_read_b128 v[234:237], v204 offset:45056
	v_mfma_f32_16x16x32_bf16 v[76:79], v[230:233], v[120:123], v[76:79]
	ds_read_b128 v[230:233], v203 offset:45056
	ds_write_b64 v184, v[130:131] offset:8192
	v_mfma_f32_16x16x32_bf16 v[76:79], v[180:183], v[116:119], v[76:79]
	ds_read_b128 v[180:183], v202 offset:45056
	v_mfma_f32_16x16x32_bf16 v[76:79], v[176:179], v[112:115], v[76:79]
	ds_read_b128 v[176:179], v201 offset:45056
	global_load_dwordx4 v[132:135], v198, s[8:9]
	s_waitcnt lgkmcnt(8)
	v_mfma_f32_16x16x32_bf16 v[80:83], v[160:163], v[96:99], 0
	v_exp_f32_e32 v64, v64
	v_exp_f32_e32 v65, v65
	v_exp_f32_e32 v66, v66
	v_mfma_f32_16x16x32_bf16 v[80:83], v[164:167], v[100:103], v[80:83]
	v_exp_f32_e32 v67, v67
	v_exp_f32_e32 v68, v68
	v_exp_f32_e32 v69, v69
	global_load_dwordx4 v[128:131], v199, s[8:9]
	v_mfma_f32_16x16x32_bf16 v[80:83], v[168:171], v[104:107], v[80:83]
	v_exp_f32_e32 v70, v70
	v_exp_f32_e32 v71, v71
	v_add_f32_e32 v194, v194, v64
	v_mfma_f32_16x16x32_bf16 v[80:83], v[172:175], v[108:111], v[80:83]
	v_add_f32_e32 v194, v194, v65
	v_add_f32_e32 v194, v194, v66
	v_add_f32_e32 v194, v194, v67
	global_load_dwordx4 v[136:139], v196, s[6:7]
	v_mfma_f32_16x16x32_bf16 v[84:87], v[172:175], v[124:127], 0
	v_add_f32_e32 v195, v195, v68
	v_add_f32_e32 v195, v195, v69
	v_add_f32_e32 v195, v195, v70
	ds_read_b128 v[172:175], v211 offset:6144
	v_mfma_f32_16x16x32_bf16 v[84:87], v[168:171], v[120:123], v[84:87]
	v_add_f32_e32 v195, v195, v71
	v_cvt_pk_bf16_f32 v64, v64, v65
	v_cvt_pk_bf16_f32 v65, v66, v67
	ds_read_b128 v[168:171], v211 offset:4096
	global_load_dwordx4 v[140:143], v197, s[6:7]
	v_mfma_f32_16x16x32_bf16 v[84:87], v[164:167], v[116:119], v[84:87]
	v_cvt_pk_bf16_f32 v68, v68, v69
	v_cvt_pk_bf16_f32 v69, v70, v71
	ds_read_b128 v[164:167], v211 offset:2048
	v_mfma_f32_16x16x32_bf16 v[84:87], v[160:163], v[112:115], v[84:87]
	ds_read_b128 v[160:163], v211 offset:0
	s_waitcnt lgkmcnt(4)
	v_mfma_f32_16x16x32_bf16 v[88:91], v[176:179], v[96:99], 0
	v_exp_f32_e32 v72, v72
	v_exp_f32_e32 v73, v73
	v_exp_f32_e32 v74, v74
	v_mfma_f32_16x16x32_bf16 v[88:91], v[180:183], v[100:103], v[88:91]
	v_exp_f32_e32 v75, v75
	v_exp_f32_e32 v76, v76
	v_exp_f32_e32 v77, v77
	v_mfma_f32_16x16x32_bf16 v[88:91], v[230:233], v[104:107], v[88:91]
	v_exp_f32_e32 v78, v78
	v_exp_f32_e32 v79, v79
	v_add_f32_e32 v194, v194, v72
	v_mfma_f32_16x16x32_bf16 v[88:91], v[234:237], v[108:111], v[88:91]
	v_add_f32_e32 v194, v194, v73
	v_add_f32_e32 v194, v194, v74
	v_add_f32_e32 v194, v194, v75
	v_mfma_f32_16x16x32_bf16 v[92:95], v[234:237], v[124:127], 0
	v_add_f32_e32 v195, v195, v76
	v_add_f32_e32 v195, v195, v77
	v_add_f32_e32 v195, v195, v78
	ds_read_b128 v[234:237], v211 offset:14336
	v_mfma_f32_16x16x32_bf16 v[92:95], v[230:233], v[120:123], v[92:95]
	v_add_f32_e32 v195, v195, v79
	v_cvt_pk_bf16_f32 v66, v72, v73
	v_cvt_pk_bf16_f32 v67, v74, v75
	ds_read_b128 v[230:233], v211 offset:12288
	v_mfma_f32_16x16x32_bf16 v[92:95], v[180:183], v[116:119], v[92:95]
	v_cvt_pk_bf16_f32 v70, v76, v77
	v_cvt_pk_bf16_f32 v71, v78, v79
	ds_read_b128 v[180:183], v211 offset:10240
	v_mfma_f32_16x16x32_bf16 v[92:95], v[176:179], v[112:115], v[92:95]
	ds_read_b128 v[176:179], v211 offset:8192
	s_waitcnt lgkmcnt(4)
	v_mfma_f32_16x16x32_bf16 v[0:3], v[160:163], v[64:67], v[0:3]
	v_exp_f32_e32 v80, v80
	v_exp_f32_e32 v81, v81
	v_exp_f32_e32 v82, v82
	v_mfma_f32_16x16x32_bf16 v[4:7], v[160:163], v[68:71], v[4:7]
	v_exp_f32_e32 v83, v83
	v_exp_f32_e32 v84, v84
	v_exp_f32_e32 v85, v85
	ds_read_b128 v[160:163], v224 offset:0
	v_mfma_f32_16x16x32_bf16 v[12:15], v[164:167], v[68:71], v[12:15]
	v_exp_f32_e32 v86, v86
	v_exp_f32_e32 v87, v87
	v_add_f32_e32 v194, v194, v80
	v_mfma_f32_16x16x32_bf16 v[8:11], v[164:167], v[64:67], v[8:11]
	v_add_f32_e32 v194, v194, v81
	v_add_f32_e32 v194, v194, v82
	v_add_f32_e32 v194, v194, v83
	ds_read_b128 v[164:167], v224 offset:2048
	v_mfma_f32_16x16x32_bf16 v[16:19], v[168:171], v[64:67], v[16:19]
	v_add_f32_e32 v195, v195, v84
	v_add_f32_e32 v195, v195, v85
	v_add_f32_e32 v195, v195, v86
	v_mfma_f32_16x16x32_bf16 v[20:23], v[168:171], v[68:71], v[20:23]
	v_add_f32_e32 v195, v195, v87
	v_cvt_pk_bf16_f32 v80, v80, v81
	v_cvt_pk_bf16_f32 v81, v82, v83
	ds_read_b128 v[168:171], v224 offset:4096
	v_mfma_f32_16x16x32_bf16 v[28:31], v[172:175], v[68:71], v[28:31]
	v_cvt_pk_bf16_f32 v84, v84, v85
	v_cvt_pk_bf16_f32 v85, v86, v87
	v_mfma_f32_16x16x32_bf16 v[24:27], v[172:175], v[64:67], v[24:27]
	ds_read_b128 v[172:175], v224 offset:6144
	s_waitcnt lgkmcnt(4)
	v_mfma_f32_16x16x32_bf16 v[32:35], v[176:179], v[64:67], v[32:35]
	v_exp_f32_e32 v88, v88
	v_exp_f32_e32 v89, v89
	v_exp_f32_e32 v90, v90
	v_mfma_f32_16x16x32_bf16 v[36:39], v[176:179], v[68:71], v[36:39]
	v_exp_f32_e32 v91, v91
	v_exp_f32_e32 v92, v92
	v_exp_f32_e32 v93, v93
	ds_read_b128 v[176:179], v224 offset:8192
	v_mfma_f32_16x16x32_bf16 v[44:47], v[180:183], v[68:71], v[44:47]
	v_exp_f32_e32 v94, v94
	v_exp_f32_e32 v95, v95
	v_add_f32_e32 v194, v194, v88
	v_mfma_f32_16x16x32_bf16 v[40:43], v[180:183], v[64:67], v[40:43]
	v_add_f32_e32 v194, v194, v89
	v_add_f32_e32 v194, v194, v90
	v_add_f32_e32 v194, v194, v91
	ds_read_b128 v[180:183], v224 offset:10240
	v_mfma_f32_16x16x32_bf16 v[48:51], v[230:233], v[64:67], v[48:51]
	v_add_f32_e32 v195, v195, v92
	v_add_f32_e32 v195, v195, v93
	v_add_f32_e32 v195, v195, v94
	v_mfma_f32_16x16x32_bf16 v[52:55], v[230:233], v[68:71], v[52:55]
	v_add_f32_e32 v195, v195, v95
	v_cvt_pk_bf16_f32 v82, v88, v89
	v_cvt_pk_bf16_f32 v83, v90, v91
	ds_read_b128 v[230:233], v224 offset:12288
	v_mfma_f32_16x16x32_bf16 v[60:63], v[234:237], v[68:71], v[60:63]
	v_cvt_pk_bf16_f32 v86, v92, v93
	v_cvt_pk_bf16_f32 v87, v94, v95
	v_mfma_f32_16x16x32_bf16 v[56:59], v[234:237], v[64:67], v[56:59]
	ds_read_b128 v[234:237], v224 offset:14336
	s_waitcnt lgkmcnt(7)
	v_mfma_f32_16x16x32_bf16 v[0:3], v[160:163], v[80:83], v[0:3]
	v_mfma_f32_16x16x32_bf16 v[4:7], v[160:163], v[84:87], v[4:7]
	ds_read_b128 v[160:163], v201 offset:49152
	s_waitcnt lgkmcnt(7)
	v_mfma_f32_16x16x32_bf16 v[12:15], v[164:167], v[84:87], v[12:15]
	v_mfma_f32_16x16x32_bf16 v[8:11], v[164:167], v[80:83], v[8:11]
	ds_read_b128 v[164:167], v202 offset:49152
	s_waitcnt lgkmcnt(7)
	v_mfma_f32_16x16x32_bf16 v[16:19], v[168:171], v[80:83], v[16:19]
	v_mfma_f32_16x16x32_bf16 v[20:23], v[168:171], v[84:87], v[20:23]
	ds_read_b128 v[168:171], v203 offset:49152
	s_waitcnt lgkmcnt(7)
	v_mfma_f32_16x16x32_bf16 v[28:31], v[172:175], v[84:87], v[28:31]
	v_mfma_f32_16x16x32_bf16 v[24:27], v[172:175], v[80:83], v[24:27]
	ds_read_b128 v[172:175], v204 offset:49152
	s_waitcnt lgkmcnt(7)
	v_mfma_f32_16x16x32_bf16 v[32:35], v[176:179], v[80:83], v[32:35]
	v_mfma_f32_16x16x32_bf16 v[36:39], v[176:179], v[84:87], v[36:39]
	ds_read_b128 v[176:179], v201 offset:53248
	s_waitcnt lgkmcnt(7)
	v_mfma_f32_16x16x32_bf16 v[44:47], v[180:183], v[84:87], v[44:47]
	v_mfma_f32_16x16x32_bf16 v[40:43], v[180:183], v[80:83], v[40:43]
	ds_read_b128 v[180:183], v202 offset:53248
	s_waitcnt lgkmcnt(7)
	v_mfma_f32_16x16x32_bf16 v[48:51], v[230:233], v[80:83], v[48:51]
	v_mfma_f32_16x16x32_bf16 v[52:55], v[230:233], v[84:87], v[52:55]
	ds_read_b128 v[230:233], v203 offset:53248
	s_waitcnt lgkmcnt(7)
	v_mfma_f32_16x16x32_bf16 v[60:63], v[234:237], v[84:87], v[60:63]
	v_mfma_f32_16x16x32_bf16 v[56:59], v[234:237], v[80:83], v[56:59]
	ds_read_b128 v[234:237], v204 offset:53248
	s_waitcnt lgkmcnt(7)
	v_mfma_f32_16x16x32_bf16 v[64:67], v[160:163], v[96:99], 0
	s_waitcnt lgkmcnt(6)
	v_mfma_f32_16x16x32_bf16 v[64:67], v[164:167], v[100:103], v[64:67]
	s_add_u32 s100, s100, 0x4000
	s_cmp_eq_u32 s100, 0x10000
	s_cselect_b32 s100, 0x24000, s100
	s_cmp_eq_u32 s100, 0x28000
	s_cselect_b32 s100, 0, s100
	s_add_u32 s101, s101, 0x4000
	s_cmp_eq_u32 s101, 0x10000
	s_cselect_b32 s101, 0x24000, s101
	s_cmp_eq_u32 s101, 0x28000
	s_cselect_b32 s101, 0, s101
	v_add_u32_e32 v211, s100, v209
	v_add_u32_e32 v224, s100, v210
	v_add_u32_e32 v229, s101, v227
	v_add_u32_e32 v184, s101, v228
	s_add_u32 s8, s16, 0x3bc00380
	s_addc_u32 s9, s17, 0
	s_add_u32 s6, s15, 0x23a70000
	s_addc_u32 s7, s14, 0
	s_waitcnt lgkmcnt(5)
	v_mfma_f32_16x16x32_bf16 v[64:67], v[168:171], v[104:107], v[64:67]
	s_waitcnt lgkmcnt(4)
	v_mfma_f32_16x16x32_bf16 v[64:67], v[172:175], v[108:111], v[64:67]
	s_waitcnt vmcnt(4)
	ds_write_b128 v225, v[152:155] offset:16384
	v_mfma_f32_16x16x32_bf16 v[68:71], v[172:175], v[124:127], 0
	ds_read_b128 v[172:175], v204 offset:57344
	v_mfma_f32_16x16x32_bf16 v[68:71], v[168:171], v[120:123], v[68:71]
	ds_read_b128 v[168:171], v203 offset:57344
	ds_write_b128 v226, v[156:159] offset:16384
	v_mfma_f32_16x16x32_bf16 v[68:71], v[164:167], v[116:119], v[68:71]
	ds_read_b128 v[164:167], v202 offset:57344
	v_mfma_f32_16x16x32_bf16 v[68:71], v[160:163], v[112:115], v[68:71]
	ds_read_b128 v[160:163], v201 offset:57344
	ds_write_b64 v229, v[148:149] offset:0
	s_waitcnt lgkmcnt(10)
	v_mfma_f32_16x16x32_bf16 v[72:75], v[176:179], v[96:99], 0
	s_waitcnt lgkmcnt(9)
	v_mfma_f32_16x16x32_bf16 v[72:75], v[180:183], v[100:103], v[72:75]
	ds_write_b64 v184, v[150:151] offset:0
	s_waitcnt lgkmcnt(9)
	v_mfma_f32_16x16x32_bf16 v[72:75], v[230:233], v[104:107], v[72:75]
	s_waitcnt lgkmcnt(8)
	v_mfma_f32_16x16x32_bf16 v[72:75], v[234:237], v[108:111], v[72:75]
	ds_write_b64 v229, v[144:145] offset:8192
	v_mfma_f32_16x16x32_bf16 v[76:79], v[234:237], v[124:127], 0
	ds_read_b128 v[234:237], v204 offset:61440
	v_mfma_f32_16x16x32_bf16 v[76:79], v[230:233], v[120:123], v[76:79]
	ds_read_b128 v[230:233], v203 offset:61440
	ds_write_b64 v184, v[146:147] offset:8192
	v_mfma_f32_16x16x32_bf16 v[76:79], v[180:183], v[116:119], v[76:79]
	ds_read_b128 v[180:183], v202 offset:61440
	v_mfma_f32_16x16x32_bf16 v[76:79], v[176:179], v[112:115], v[76:79]
	ds_read_b128 v[176:179], v201 offset:61440
	global_load_dwordx4 v[148:151], v198, s[8:9]
	s_waitcnt lgkmcnt(8)
	v_mfma_f32_16x16x32_bf16 v[80:83], v[160:163], v[96:99], 0
	v_exp_f32_e32 v64, v64
	v_exp_f32_e32 v65, v65
	v_exp_f32_e32 v66, v66
	v_mfma_f32_16x16x32_bf16 v[80:83], v[164:167], v[100:103], v[80:83]
	v_exp_f32_e32 v67, v67
	v_exp_f32_e32 v68, v68
	v_exp_f32_e32 v69, v69
	global_load_dwordx4 v[144:147], v199, s[8:9]
	v_mfma_f32_16x16x32_bf16 v[80:83], v[168:171], v[104:107], v[80:83]
	v_exp_f32_e32 v70, v70
	v_exp_f32_e32 v71, v71
	v_add_f32_e32 v194, v194, v64
	v_mfma_f32_16x16x32_bf16 v[80:83], v[172:175], v[108:111], v[80:83]
	v_add_f32_e32 v194, v194, v65
	v_add_f32_e32 v194, v194, v66
	v_add_f32_e32 v194, v194, v67
	global_load_dwordx4 v[152:155], v196, s[6:7]
	v_mfma_f32_16x16x32_bf16 v[84:87], v[172:175], v[124:127], 0
	v_add_f32_e32 v195, v195, v68
	v_add_f32_e32 v195, v195, v69
	v_add_f32_e32 v195, v195, v70
	ds_read_b128 v[172:175], v211 offset:6144
	v_mfma_f32_16x16x32_bf16 v[84:87], v[168:171], v[120:123], v[84:87]
	v_add_f32_e32 v195, v195, v71
	v_cvt_pk_bf16_f32 v64, v64, v65
	v_cvt_pk_bf16_f32 v65, v66, v67
	ds_read_b128 v[168:171], v211 offset:4096
	global_load_dwordx4 v[156:159], v197, s[6:7]
	v_mfma_f32_16x16x32_bf16 v[84:87], v[164:167], v[116:119], v[84:87]
	v_cvt_pk_bf16_f32 v68, v68, v69
	v_cvt_pk_bf16_f32 v69, v70, v71
	ds_read_b128 v[164:167], v211 offset:2048
	v_mfma_f32_16x16x32_bf16 v[84:87], v[160:163], v[112:115], v[84:87]
	ds_read_b128 v[160:163], v211 offset:0
	s_waitcnt lgkmcnt(4)
	v_mfma_f32_16x16x32_bf16 v[88:91], v[176:179], v[96:99], 0
	v_exp_f32_e32 v72, v72
	v_exp_f32_e32 v73, v73
	v_exp_f32_e32 v74, v74
	v_mfma_f32_16x16x32_bf16 v[88:91], v[180:183], v[100:103], v[88:91]
	v_exp_f32_e32 v75, v75
	v_exp_f32_e32 v76, v76
	v_exp_f32_e32 v77, v77
	s_add_u32 s10, s10, 0x200
	s_addc_u32 s11, s11, 0
	s_add_u32 s12, s12, 0x40000
	s_addc_u32 s13, s13, 0
	s_add_i32 s4, s4, 4
	s_cmpk_lt_u32 s4, 0x104
	s_cselect_b64 s[6:7], -1, 0
	s_and_b64 s[6:7], s[0:1], s[6:7]
	s_and_b64 vcc, exec, s[6:7]
	v_mfma_f32_16x16x32_bf16 v[88:91], v[230:233], v[104:107], v[88:91]
	v_exp_f32_e32 v78, v78
	v_exp_f32_e32 v79, v79
	v_add_f32_e32 v194, v194, v72
	v_mfma_f32_16x16x32_bf16 v[88:91], v[234:237], v[108:111], v[88:91]
	v_add_f32_e32 v194, v194, v73
	v_add_f32_e32 v194, v194, v74
	v_add_f32_e32 v194, v194, v75
	v_mfma_f32_16x16x32_bf16 v[92:95], v[234:237], v[124:127], 0
	v_add_f32_e32 v195, v195, v76
	v_add_f32_e32 v195, v195, v77
	v_add_f32_e32 v195, v195, v78
	ds_read_b128 v[234:237], v211 offset:14336
	v_mfma_f32_16x16x32_bf16 v[92:95], v[230:233], v[120:123], v[92:95]
	v_add_f32_e32 v195, v195, v79
	v_cvt_pk_bf16_f32 v66, v72, v73
	v_cvt_pk_bf16_f32 v67, v74, v75
	ds_read_b128 v[230:233], v211 offset:12288
	v_mfma_f32_16x16x32_bf16 v[92:95], v[180:183], v[116:119], v[92:95]
	v_cvt_pk_bf16_f32 v70, v76, v77
	v_cvt_pk_bf16_f32 v71, v78, v79
	ds_read_b128 v[180:183], v211 offset:10240
	v_mfma_f32_16x16x32_bf16 v[92:95], v[176:179], v[112:115], v[92:95]
	ds_read_b128 v[176:179], v211 offset:8192
	s_cbranch_vccnz .Lattn_L_top
	s_waitcnt lgkmcnt(4)
	v_mfma_f32_16x16x32_bf16 v[0:3], v[160:163], v[64:67], v[0:3]
	v_exp_f32_e32 v80, v80
	v_exp_f32_e32 v81, v81
	v_exp_f32_e32 v82, v82
	v_mfma_f32_16x16x32_bf16 v[4:7], v[160:163], v[68:71], v[4:7]
	v_exp_f32_e32 v83, v83
	v_exp_f32_e32 v84, v84
	v_exp_f32_e32 v85, v85
	ds_read_b128 v[160:163], v224 offset:0
	v_mfma_f32_16x16x32_bf16 v[12:15], v[164:167], v[68:71], v[12:15]
	v_exp_f32_e32 v86, v86
	v_exp_f32_e32 v87, v87
	v_add_f32_e32 v194, v194, v80
	v_mfma_f32_16x16x32_bf16 v[8:11], v[164:167], v[64:67], v[8:11]
	v_add_f32_e32 v194, v194, v81
	v_add_f32_e32 v194, v194, v82
	v_add_f32_e32 v194, v194, v83
	ds_read_b128 v[164:167], v224 offset:2048
	v_mfma_f32_16x16x32_bf16 v[16:19], v[168:171], v[64:67], v[16:19]
	v_add_f32_e32 v195, v195, v84
	v_add_f32_e32 v195, v195, v85
	v_add_f32_e32 v195, v195, v86
	v_mfma_f32_16x16x32_bf16 v[20:23], v[168:171], v[68:71], v[20:23]
	v_add_f32_e32 v195, v195, v87
	v_cvt_pk_bf16_f32 v80, v80, v81
	v_cvt_pk_bf16_f32 v81, v82, v83
	ds_read_b128 v[168:171], v224 offset:4096
	v_mfma_f32_16x16x32_bf16 v[28:31], v[172:175], v[68:71], v[28:31]
	v_cvt_pk_bf16_f32 v84, v84, v85
	v_cvt_pk_bf16_f32 v85, v86, v87
	v_mfma_f32_16x16x32_bf16 v[24:27], v[172:175], v[64:67], v[24:27]
	ds_read_b128 v[172:175], v224 offset:6144
	s_waitcnt lgkmcnt(4)
	v_mfma_f32_16x16x32_bf16 v[32:35], v[176:179], v[64:67], v[32:35]
	v_exp_f32_e32 v88, v88
	v_exp_f32_e32 v89, v89
	v_exp_f32_e32 v90, v90
	v_mfma_f32_16x16x32_bf16 v[36:39], v[176:179], v[68:71], v[36:39]
	v_exp_f32_e32 v91, v91
	v_exp_f32_e32 v92, v92
	v_exp_f32_e32 v93, v93
	ds_read_b128 v[176:179], v224 offset:8192
	v_mfma_f32_16x16x32_bf16 v[44:47], v[180:183], v[68:71], v[44:47]
	v_exp_f32_e32 v94, v94
	v_exp_f32_e32 v95, v95
	v_add_f32_e32 v194, v194, v88
	v_mfma_f32_16x16x32_bf16 v[40:43], v[180:183], v[64:67], v[40:43]
	v_add_f32_e32 v194, v194, v89
	v_add_f32_e32 v194, v194, v90
	v_add_f32_e32 v194, v194, v91
	ds_read_b128 v[180:183], v224 offset:10240
	v_mfma_f32_16x16x32_bf16 v[48:51], v[230:233], v[64:67], v[48:51]
	v_add_f32_e32 v195, v195, v92
	v_add_f32_e32 v195, v195, v93
	v_add_f32_e32 v195, v195, v94
	v_mfma_f32_16x16x32_bf16 v[52:55], v[230:233], v[68:71], v[52:55]
	v_add_f32_e32 v195, v195, v95
	v_cvt_pk_bf16_f32 v82, v88, v89
	v_cvt_pk_bf16_f32 v83, v90, v91
	ds_read_b128 v[230:233], v224 offset:12288
	v_mfma_f32_16x16x32_bf16 v[60:63], v[234:237], v[68:71], v[60:63]
	v_cvt_pk_bf16_f32 v86, v92, v93
	v_cvt_pk_bf16_f32 v87, v94, v95
	v_mfma_f32_16x16x32_bf16 v[56:59], v[234:237], v[64:67], v[56:59]
	ds_read_b128 v[234:237], v224 offset:14336
	s_waitcnt lgkmcnt(7)
	v_mfma_f32_16x16x32_bf16 v[0:3], v[160:163], v[80:83], v[0:3]
	v_mfma_f32_16x16x32_bf16 v[4:7], v[160:163], v[84:87], v[4:7]
	s_waitcnt lgkmcnt(6)
	v_mfma_f32_16x16x32_bf16 v[12:15], v[164:167], v[84:87], v[12:15]
	v_mfma_f32_16x16x32_bf16 v[8:11], v[164:167], v[80:83], v[8:11]
	s_waitcnt lgkmcnt(5)
	v_mfma_f32_16x16x32_bf16 v[16:19], v[168:171], v[80:83], v[16:19]
	v_mfma_f32_16x16x32_bf16 v[20:23], v[168:171], v[84:87], v[20:23]
	s_waitcnt lgkmcnt(4)
	v_mfma_f32_16x16x32_bf16 v[28:31], v[172:175], v[84:87], v[28:31]
	v_mfma_f32_16x16x32_bf16 v[24:27], v[172:175], v[80:83], v[24:27]
	s_waitcnt lgkmcnt(3)
	v_mfma_f32_16x16x32_bf16 v[32:35], v[176:179], v[80:83], v[32:35]
	v_mfma_f32_16x16x32_bf16 v[36:39], v[176:179], v[84:87], v[36:39]
	s_waitcnt lgkmcnt(2)
	v_mfma_f32_16x16x32_bf16 v[44:47], v[180:183], v[84:87], v[44:47]
	v_mfma_f32_16x16x32_bf16 v[40:43], v[180:183], v[80:83], v[40:43]
	s_waitcnt lgkmcnt(1)
	v_mfma_f32_16x16x32_bf16 v[48:51], v[230:233], v[80:83], v[48:51]
	v_mfma_f32_16x16x32_bf16 v[52:55], v[230:233], v[84:87], v[52:55]
	s_waitcnt lgkmcnt(0)
	v_mfma_f32_16x16x32_bf16 v[60:63], v[234:237], v[84:87], v[60:63]
	v_mfma_f32_16x16x32_bf16 v[56:59], v[234:237], v[80:83], v[56:59]
.Lattn_epi:
	s_waitcnt vmcnt(0)
	s_nop 7
	s_nop 7
	ds_swizzle_b32 v64, v194 offset:swizzle(SWAP,16)
	s_waitcnt lgkmcnt(0)
	v_add_f32_e32 v194, v194, v64
	v_mov_b32_e32 v65, v194
	s_nop 1
	v_permlane32_swap_b32_e32 v194, v65
	v_add_f32_e32 v194, v194, v65
	s_nop 0
	v_rcp_f32_e32 v66, v194
	ds_swizzle_b32 v64, v195 offset:swizzle(SWAP,16)
	s_waitcnt lgkmcnt(0)
	v_add_f32_e32 v195, v195, v64
	v_mov_b32_e32 v65, v195
	s_nop 1
	v_permlane32_swap_b32_e32 v195, v65
	v_add_f32_e32 v195, v195, v65
	s_nop 0
	v_rcp_f32_e32 v67, v195
	v_readlane_b32 s6, v250, 8
	v_mbcnt_lo_u32_b32 v68, -1, 0
	v_mbcnt_hi_u32_b32 v68, -1, v68
	v_and_b32_e32 v69, 15, v68
	v_lshrrev_b32_e32 v70, 4, v68
	s_lshr_b32 s7, s6, 1
	v_add_u32_e32 v69, s7, v69
	v_lshlrev_b32_e32 v69, 12, v69
	v_and_b32_e32 v71, 1, v70
	v_lshlrev_b32_e32 v71, 5, v71
	v_and_b32_e32 v70, 2, v70
	v_lshl_add_u32 v71, v70, 3, v71
	v_add_u32_e32 v70, v69, v71
	v_add_u32_e32 v71, 0x10000, v70
	v_mul_f32_e32 v0, v0, v66
	v_mul_f32_e32 v1, v1, v66
	v_mul_f32_e32 v2, v2, v66
	v_mul_f32_e32 v3, v3, v66
	v_mul_f32_e32 v8, v8, v66
	v_mul_f32_e32 v9, v9, v66
	v_mul_f32_e32 v10, v10, v66
	v_mul_f32_e32 v11, v11, v66
	v_cvt_pk_bf16_f32 v72, v0, v1
	v_cvt_pk_bf16_f32 v73, v2, v3
	v_cvt_pk_bf16_f32 v74, v8, v9
	v_cvt_pk_bf16_f32 v75, v10, v11
	s_nop 1
	v_permlane16_swap_b32_e32 v72, v74
	v_permlane16_swap_b32_e32 v73, v75
	s_nop 1
	global_store_dwordx4 v70, v[72:75], s[58:59] offset:0
	v_mul_f32_e32 v16, v16, v66
	v_mul_f32_e32 v17, v17, v66
	v_mul_f32_e32 v18, v18, v66
	v_mul_f32_e32 v19, v19, v66
	v_mul_f32_e32 v24, v24, v66
	v_mul_f32_e32 v25, v25, v66
	v_mul_f32_e32 v26, v26, v66
	v_mul_f32_e32 v27, v27, v66
	v_cvt_pk_bf16_f32 v76, v16, v17
	v_cvt_pk_bf16_f32 v77, v18, v19
	v_cvt_pk_bf16_f32 v78, v24, v25
	v_cvt_pk_bf16_f32 v79, v26, v27
	s_nop 1
	v_permlane16_swap_b32_e32 v76, v78
	v_permlane16_swap_b32_e32 v77, v79
	s_nop 1
	global_store_dwordx4 v70, v[76:79], s[58:59] offset:64
	v_mul_f32_e32 v32, v32, v66
	v_mul_f32_e32 v33, v33, v66
	v_mul_f32_e32 v34, v34, v66
	v_mul_f32_e32 v35, v35, v66
	v_mul_f32_e32 v40, v40, v66
	v_mul_f32_e32 v41, v41, v66
	v_mul_f32_e32 v42, v42, v66
	v_mul_f32_e32 v43, v43, v66
	v_cvt_pk_bf16_f32 v80, v32, v33
	v_cvt_pk_bf16_f32 v81, v34, v35
	v_cvt_pk_bf16_f32 v82, v40, v41
	v_cvt_pk_bf16_f32 v83, v42, v43
	s_nop 1
	v_permlane16_swap_b32_e32 v80, v82
	v_permlane16_swap_b32_e32 v81, v83
	s_nop 1
	global_store_dwordx4 v70, v[80:83], s[58:59] offset:128
	v_mul_f32_e32 v48, v48, v66
	v_mul_f32_e32 v49, v49, v66
	v_mul_f32_e32 v50, v50, v66
	v_mul_f32_e32 v51, v51, v66
	v_mul_f32_e32 v56, v56, v66
	v_mul_f32_e32 v57, v57, v66
	v_mul_f32_e32 v58, v58, v66
	v_mul_f32_e32 v59, v59, v66
	v_cvt_pk_bf16_f32 v84, v48, v49
	v_cvt_pk_bf16_f32 v85, v50, v51
	v_cvt_pk_bf16_f32 v86, v56, v57
	v_cvt_pk_bf16_f32 v87, v58, v59
	s_nop 1
	v_permlane16_swap_b32_e32 v84, v86
	v_permlane16_swap_b32_e32 v85, v87
	s_nop 1
	global_store_dwordx4 v70, v[84:87], s[58:59] offset:192
	v_mul_f32_e32 v4, v4, v67
	v_mul_f32_e32 v5, v5, v67
	v_mul_f32_e32 v6, v6, v67
	v_mul_f32_e32 v7, v7, v67
	v_mul_f32_e32 v12, v12, v67
	v_mul_f32_e32 v13, v13, v67
	v_mul_f32_e32 v14, v14, v67
	v_mul_f32_e32 v15, v15, v67
	v_cvt_pk_bf16_f32 v88, v4, v5
	v_cvt_pk_bf16_f32 v89, v6, v7
	v_cvt_pk_bf16_f32 v90, v12, v13
	v_cvt_pk_bf16_f32 v91, v14, v15
	s_nop 1
	v_permlane16_swap_b32_e32 v88, v90
	v_permlane16_swap_b32_e32 v89, v91
	s_nop 1
	global_store_dwordx4 v71, v[88:91], s[58:59] offset:0
	v_mul_f32_e32 v20, v20, v67
	v_mul_f32_e32 v21, v21, v67
	v_mul_f32_e32 v22, v22, v67
	v_mul_f32_e32 v23, v23, v67
	v_mul_f32_e32 v28, v28, v67
	v_mul_f32_e32 v29, v29, v67
	v_mul_f32_e32 v30, v30, v67
	v_mul_f32_e32 v31, v31, v67
	v_cvt_pk_bf16_f32 v92, v20, v21
	v_cvt_pk_bf16_f32 v93, v22, v23
	v_cvt_pk_bf16_f32 v94, v28, v29
	v_cvt_pk_bf16_f32 v95, v30, v31
	s_nop 1
	v_permlane16_swap_b32_e32 v92, v94
	v_permlane16_swap_b32_e32 v93, v95
	s_nop 1
	global_store_dwordx4 v71, v[92:95], s[58:59] offset:64
	v_mul_f32_e32 v36, v36, v67
	v_mul_f32_e32 v37, v37, v67
	v_mul_f32_e32 v38, v38, v67
	v_mul_f32_e32 v39, v39, v67
	v_mul_f32_e32 v44, v44, v67
	v_mul_f32_e32 v45, v45, v67
	v_mul_f32_e32 v46, v46, v67
	v_mul_f32_e32 v47, v47, v67
	v_cvt_pk_bf16_f32 v72, v36, v37
	v_cvt_pk_bf16_f32 v73, v38, v39
	v_cvt_pk_bf16_f32 v74, v44, v45
	v_cvt_pk_bf16_f32 v75, v46, v47
	s_nop 1
	v_permlane16_swap_b32_e32 v72, v74
	v_permlane16_swap_b32_e32 v73, v75
	s_nop 1
	global_store_dwordx4 v71, v[72:75], s[58:59] offset:128
	v_mul_f32_e32 v52, v52, v67
	v_mul_f32_e32 v53, v53, v67
	v_mul_f32_e32 v54, v54, v67
	v_mul_f32_e32 v55, v55, v67
	v_mul_f32_e32 v60, v60, v67
	v_mul_f32_e32 v61, v61, v67
	v_mul_f32_e32 v62, v62, v67
	v_mul_f32_e32 v63, v63, v67
	v_cvt_pk_bf16_f32 v76, v52, v53
	v_cvt_pk_bf16_f32 v77, v54, v55
	v_cvt_pk_bf16_f32 v78, v60, v61
	v_cvt_pk_bf16_f32 v79, v62, v63
	s_nop 1
	v_permlane16_swap_b32_e32 v76, v78
	v_permlane16_swap_b32_e32 v77, v79
	s_nop 1
	global_store_dwordx4 v71, v[76:79], s[58:59] offset:192
	s_barrier

	.amdhsa_kernel _Z6mk_fwd4Args
		.amdhsa_group_segment_fixed_size 16384
		.amdhsa_private_segment_fixed_size 0
		.amdhsa_kernarg_size 464
		.amdhsa_user_sgpr_count 2
		.amdhsa_user_sgpr_dispatch_ptr 0
		.amdhsa_user_sgpr_queue_ptr 0
		.amdhsa_user_sgpr_kernarg_segment_ptr 1
		.amdhsa_user_sgpr_dispatch_id 0
		.amdhsa_user_sgpr_kernarg_preload_length 0
		.amdhsa_user_sgpr_kernarg_preload_offset 0
		.amdhsa_user_sgpr_private_segment_size 0
		.amdhsa_uses_dynamic_stack 0
		.amdhsa_enable_private_segment 0
		.amdhsa_system_sgpr_workgroup_id_x 1
		.amdhsa_system_sgpr_workgroup_id_y 0
		.amdhsa_system_sgpr_workgroup_id_z 0
		.amdhsa_system_sgpr_workgroup_info 0
		.amdhsa_system_vgpr_workitem_id 0
		.amdhsa_next_free_vgpr 256
		.amdhsa_next_free_sgpr 102
		.amdhsa_accum_offset 256
		.amdhsa_reserve_vcc 1
		.amdhsa_float_round_mode_32 0
		.amdhsa_float_round_mode_16_64 0
		.amdhsa_float_denorm_mode_32 3
		.amdhsa_float_denorm_mode_16_64 3
		.amdhsa_dx10_clamp 1
		.amdhsa_ieee_mode 1
		.amdhsa_fp16_overflow 0
		.amdhsa_tg_split 0
		.amdhsa_exception_fp_ieee_invalid_op 0
		.amdhsa_exception_fp_denorm_src 0
		.amdhsa_exception_fp_ieee_div_zero 0
		.amdhsa_exception_fp_ieee_overflow 0
		.amdhsa_exception_fp_ieee_underflow 0
		.amdhsa_exception_fp_ieee_inexact 0
		.amdhsa_exception_int_div_zero 0
	.end_amdhsa_kernel

amdhsa.kernels:
  - .agpr_count:     0
    .args:
      - .offset:         0
        .size:           208
        .value_kind:     by_value
      - .offset:         208
        .size:           4
        .value_kind:     hidden_block_count_x
      - .offset:         212
        .size:           4
        .value_kind:     hidden_block_count_y
      - .offset:         216
        .size:           4
        .value_kind:     hidden_block_count_z
      - .offset:         220
        .size:           2
        .value_kind:     hidden_group_size_x
      - .offset:         222
        .size:           2
        .value_kind:     hidden_group_size_y
      - .offset:         224
        .size:           2
        .value_kind:     hidden_group_size_z
      - .offset:         226
        .size:           2
        .value_kind:     hidden_remainder_x
      - .offset:         228
        .size:           2
        .value_kind:     hidden_remainder_y
      - .offset:         230
        .size:           2
        .value_kind:     hidden_remainder_z
      - .offset:         248
        .size:           8
        .value_kind:     hidden_global_offset_x
      - .offset:         256
        .size:           8
        .value_kind:     hidden_global_offset_y
      - .offset:         264
        .size:           8
        .value_kind:     hidden_global_offset_z
      - .offset:         272
        .size:           2
        .value_kind:     hidden_grid_dims
      - .offset:         328
        .size:           4
        .value_kind:     hidden_dynamic_lds_size
    .group_segment_fixed_size: 16384
    .kernarg_segment_align: 8
    .kernarg_segment_size: 464
    .language:       OpenCL C
    .language_version:
      - 2
      - 0
    .max_flat_workgroup_size: 512
    .name:           _Z6mk_fwd4Args
    .private_segment_fixed_size: 0
    .sgpr_count:     108
    .sgpr_spill_count: 449
    .symbol:         _Z6mk_fwd4Args.kd
    .uniform_work_group_size: 1
    .uses_dynamic_stack: false
    .vgpr_count:     256
    .vgpr_spill_count: 0
    .wavefront_size: 64
